# NSA tile loop trims: no canonicalising v_max, short wave-uniform branch tests, direct instance exits, one-add V base
# speedup vs baseline: 1.0108x; 1.0022x over previous
.LBB0_572:
	v_lshlrev_b32_e32 v202, 10, v3
	v_lshlrev_b32_e32 v203, 4, v198
	v_add3_u32 v69, 0, v202, v203
	ds_read_b128 v[4:7], v69
	ds_read_b128 v[8:11], v69 offset:512
	s_mov_b32 s0, 0xf149f2ca
	v_ashrrev_i32_e32 v182, 3, v68
	s_waitcnt lgkmcnt(1)
	v_mfma_f32_32x32x16_bf16 v[52:67], v[4:7], v[158:161], 0
	s_cmp_lt_i32 s82, 0
	s_waitcnt lgkmcnt(0)
	v_mfma_f32_32x32x16_bf16 v[36:51], v[8:11], v[158:161], 0
	ds_read_b128 v[4:7], v69 offset:2048
	ds_read_b128 v[8:11], v69 offset:2560
	s_waitcnt lgkmcnt(1)
	v_mfma_f32_32x32x16_bf16 v[52:67], v[4:7], v[154:157], v[52:67]
	s_waitcnt lgkmcnt(0)
	v_mfma_f32_32x32x16_bf16 v[36:51], v[8:11], v[154:157], v[36:51]
	ds_read_b128 v[4:7], v69 offset:4096
	ds_read_b128 v[8:11], v69 offset:4608
	s_waitcnt lgkmcnt(1)
	v_mfma_f32_32x32x16_bf16 v[52:67], v[4:7], v[150:153], v[52:67]
	s_waitcnt lgkmcnt(0)
	v_mfma_f32_32x32x16_bf16 v[36:51], v[8:11], v[150:153], v[36:51]
	ds_read_b128 v[4:7], v69 offset:6144
	ds_read_b128 v[8:11], v69 offset:6656
	s_waitcnt lgkmcnt(1)
	v_mfma_f32_32x32x16_bf16 v[52:67], v[4:7], v[146:149], v[52:67]
	s_waitcnt lgkmcnt(0)
	v_mfma_f32_32x32x16_bf16 v[36:51], v[8:11], v[146:149], v[36:51]
	ds_read_b128 v[4:7], v69 offset:16384
	ds_read_b128 v[8:11], v69 offset:16896
	ds_read_b128 v[74:77], v69 offset:18432
	ds_read_b128 v[78:81], v69 offset:18944
	s_waitcnt lgkmcnt(3)
	v_mfma_f32_32x32x16_bf16 v[20:35], v[4:7], v[158:161], 0
	s_waitcnt lgkmcnt(2)
	v_mfma_f32_32x32x16_bf16 v[4:19], v[8:11], v[158:161], 0
	s_waitcnt lgkmcnt(1)
	v_mfma_f32_32x32x16_bf16 v[20:35], v[74:77], v[154:157], v[20:35]
	s_waitcnt lgkmcnt(0)
	v_mfma_f32_32x32x16_bf16 v[4:19], v[78:81], v[154:157], v[4:19]
	ds_read_b128 v[74:77], v69 offset:20480
	ds_read_b128 v[78:81], v69 offset:20992
	s_waitcnt lgkmcnt(1)
	v_mfma_f32_32x32x16_bf16 v[20:35], v[74:77], v[150:153], v[20:35]
	s_waitcnt lgkmcnt(0)
	v_mfma_f32_32x32x16_bf16 v[4:19], v[78:81], v[150:153], v[4:19]
	ds_read_b128 v[74:77], v69 offset:22528
	ds_read_b128 v[78:81], v69 offset:23040
	v_lshlrev_b32_e32 v69, 6, v3
	v_sub_u32_e32 v69, v72, v69
	v_subrev_u32_e32 v72, 31, v69
	v_cmp_lt_i32_e32 vcc, -1, v72
	s_nop 1
	v_cndmask_b32_e32 v52, v195, v52, vcc
	v_cmp_lt_i32_e32 vcc, 15, v72
	s_waitcnt lgkmcnt(1)
	v_mfma_f32_32x32x16_bf16 v[20:35], v[74:77], v[146:149], v[20:35]
	v_cndmask_b32_e32 v53, v195, v53, vcc
	v_cmp_lt_i32_e32 vcc, 31, v72
	v_max3_f32 v69, v52, s0, v53
	s_movk_i32 s0, 0x7f
	v_cndmask_b32_e32 v54, v195, v54, vcc
	v_cmp_lt_i32_e32 vcc, 47, v72
	s_waitcnt lgkmcnt(0)
	v_mfma_f32_32x32x16_bf16 v[4:19], v[78:81], v[146:149], v[4:19]
	v_cndmask_b32_e32 v55, v195, v55, vcc
	v_cmp_lt_i32_e32 vcc, s0, v72
	s_movk_i32 s0, 0x8f
	v_max3_f32 v69, v69, v54, v55
	v_cndmask_b32_e32 v73, v195, v56, vcc
	v_cmp_lt_i32_e32 vcc, s0, v72
	s_movk_i32 s0, 0x9f
	s_nop 0
	v_cndmask_b32_e32 v74, v195, v57, vcc
	v_cmp_lt_i32_e32 vcc, s0, v72
	s_movk_i32 s0, 0xaf
	v_max3_f32 v56, v69, v73, v74
	v_cndmask_b32_e32 v75, v195, v58, vcc
	v_cmp_lt_i32_e32 vcc, s0, v72
	s_movk_i32 s0, 0xff
	s_nop 0
	v_cndmask_b32_e32 v76, v195, v59, vcc
	v_cmp_lt_i32_e32 vcc, s0, v72
	s_movk_i32 s0, 0x10f
	v_max3_f32 v56, v56, v75, v76
	v_cndmask_b32_e32 v77, v195, v60, vcc
	v_cmp_lt_i32_e32 vcc, s0, v72
	s_movk_i32 s0, 0x11f
	s_nop 0
	v_cndmask_b32_e32 v78, v195, v61, vcc
	v_cmp_lt_i32_e32 vcc, s0, v72
	s_movk_i32 s0, 0x12f
	v_max3_f32 v56, v56, v77, v78
	v_cndmask_b32_e32 v79, v195, v62, vcc
	v_cmp_lt_i32_e32 vcc, s0, v72
	s_movk_i32 s0, 0x17f
	s_nop 0
	v_cndmask_b32_e32 v80, v195, v63, vcc
	v_cmp_lt_i32_e32 vcc, s0, v72
	s_movk_i32 s0, 0x18f
	v_max3_f32 v56, v56, v79, v80
	v_cndmask_b32_e32 v81, v195, v64, vcc
	v_cmp_lt_i32_e32 vcc, s0, v72
	s_movk_i32 s0, 0x19f
	s_nop 0
	v_cndmask_b32_e32 v82, v195, v65, vcc
	v_cmp_lt_i32_e32 vcc, s0, v72
	s_movk_i32 s0, 0x1af
	v_max3_f32 v56, v56, v81, v82
	v_cndmask_b32_e32 v83, v195, v66, vcc
	v_cmp_lt_i32_e32 vcc, s0, v72
	s_movk_i32 s0, 0x1ff
	s_nop 0
	v_cndmask_b32_e32 v84, v195, v67, vcc
	v_cmp_lt_i32_e32 vcc, s0, v72
	s_movk_i32 s0, 0x20f
	v_max3_f32 v56, v56, v83, v84
	v_cndmask_b32_e32 v36, v195, v36, vcc
	v_cmp_lt_i32_e32 vcc, s0, v72
	s_movk_i32 s0, 0x21f
	s_nop 0
	v_cndmask_b32_e32 v37, v195, v37, vcc
	v_cmp_lt_i32_e32 vcc, s0, v72
	s_movk_i32 s0, 0x22f
	v_max3_f32 v56, v56, v36, v37
	v_cndmask_b32_e32 v38, v195, v38, vcc
	v_cmp_lt_i32_e32 vcc, s0, v72
	s_movk_i32 s0, 0x27f
	s_nop 0
	v_cndmask_b32_e32 v39, v195, v39, vcc
	v_cmp_lt_i32_e32 vcc, s0, v72
	s_movk_i32 s0, 0x28f
	v_max3_f32 v56, v56, v38, v39
	v_cndmask_b32_e32 v40, v195, v40, vcc
	v_cmp_lt_i32_e32 vcc, s0, v72
	s_movk_i32 s0, 0x29f
	s_nop 0
	v_cndmask_b32_e32 v41, v195, v41, vcc
	v_cmp_lt_i32_e32 vcc, s0, v72
	s_movk_i32 s0, 0x2af
	v_max3_f32 v56, v56, v40, v41
	v_cndmask_b32_e32 v42, v195, v42, vcc
	v_cmp_lt_i32_e32 vcc, s0, v72
	s_movk_i32 s0, 0x2ff
	s_nop 0
	v_cndmask_b32_e32 v43, v195, v43, vcc
	v_cmp_lt_i32_e32 vcc, s0, v72
	s_movk_i32 s0, 0x30f
	v_max3_f32 v56, v56, v42, v43
	v_cndmask_b32_e32 v44, v195, v44, vcc
	v_cmp_lt_i32_e32 vcc, s0, v72
	s_movk_i32 s0, 0x31f
	s_nop 0
	v_cndmask_b32_e32 v45, v195, v45, vcc
	v_cmp_lt_i32_e32 vcc, s0, v72
	s_movk_i32 s0, 0x32f
	v_max3_f32 v56, v56, v44, v45
	v_cndmask_b32_e32 v46, v195, v46, vcc
	v_cmp_lt_i32_e32 vcc, s0, v72
	s_movk_i32 s0, 0x37f
	s_nop 0
	v_cndmask_b32_e32 v47, v195, v47, vcc
	v_cmp_lt_i32_e32 vcc, s0, v72
	s_movk_i32 s0, 0x38f
	v_max3_f32 v56, v56, v46, v47
	v_cndmask_b32_e32 v48, v195, v48, vcc
	v_cmp_lt_i32_e32 vcc, s0, v72
	s_movk_i32 s0, 0x39f
	s_nop 0
	v_cndmask_b32_e32 v49, v195, v49, vcc
	v_cmp_lt_i32_e32 vcc, s0, v72
	s_movk_i32 s0, 0x3af
	v_max3_f32 v56, v56, v48, v49
	v_cndmask_b32_e32 v50, v195, v50, vcc
	v_cmp_lt_i32_e32 vcc, s0, v72
	s_movk_i32 s0, 0x40f
	s_nop 0
	v_cndmask_b32_e32 v51, v195, v51, vcc
	v_cmp_lt_i32_e32 vcc, s39, v72
	v_max3_f32 v56, v56, v50, v51
	s_nop 0
	v_cndmask_b32_e32 v85, v195, v20, vcc
	v_cmp_lt_i32_e32 vcc, s0, v72
	s_movk_i32 s0, 0x41f
	s_nop 0
	v_cndmask_b32_e32 v86, v195, v21, vcc
	v_cmp_lt_i32_e32 vcc, s0, v72
	s_movk_i32 s0, 0x42f
	v_max3_f32 v20, v56, v85, v86
	v_cndmask_b32_e32 v87, v195, v22, vcc
	v_cmp_lt_i32_e32 vcc, s0, v72
	s_movk_i32 s0, 0x47f
	s_nop 0
	v_cndmask_b32_e32 v88, v195, v23, vcc
	v_cmp_lt_i32_e32 vcc, s0, v72
	s_movk_i32 s0, 0x48f
	v_max3_f32 v20, v20, v87, v88
	v_cndmask_b32_e32 v89, v195, v24, vcc
	v_cmp_lt_i32_e32 vcc, s0, v72
	s_movk_i32 s0, 0x49f
	s_nop 0
	v_cndmask_b32_e32 v90, v195, v25, vcc
	v_cmp_lt_i32_e32 vcc, s0, v72
	s_movk_i32 s0, 0x4af
	v_max3_f32 v20, v20, v89, v90
	v_cndmask_b32_e32 v91, v195, v26, vcc
	v_cmp_lt_i32_e32 vcc, s0, v72
	s_movk_i32 s0, 0x4ff
	s_nop 0
	v_cndmask_b32_e32 v92, v195, v27, vcc
	v_cmp_lt_i32_e32 vcc, s0, v72
	s_movk_i32 s0, 0x50f
	v_max3_f32 v20, v20, v91, v92
	v_cndmask_b32_e32 v93, v195, v28, vcc
	v_cmp_lt_i32_e32 vcc, s0, v72
	s_movk_i32 s0, 0x51f
	s_nop 0
	v_cndmask_b32_e32 v94, v195, v29, vcc
	v_cmp_lt_i32_e32 vcc, s0, v72
	s_movk_i32 s0, 0x52f
	v_max3_f32 v20, v20, v93, v94
	v_cndmask_b32_e32 v95, v195, v30, vcc
	v_cmp_lt_i32_e32 vcc, s0, v72
	s_movk_i32 s0, 0x57f
	s_nop 0
	v_cndmask_b32_e32 v96, v195, v31, vcc
	v_cmp_lt_i32_e32 vcc, s0, v72
	s_movk_i32 s0, 0x58f
	v_max3_f32 v20, v20, v95, v96
	v_cndmask_b32_e32 v97, v195, v32, vcc
	v_cmp_lt_i32_e32 vcc, s0, v72
	s_movk_i32 s0, 0x59f
	s_nop 0
	v_cndmask_b32_e32 v98, v195, v33, vcc
	v_cmp_lt_i32_e32 vcc, s0, v72
	s_movk_i32 s0, 0x5af
	v_max3_f32 v20, v20, v97, v98
	v_cndmask_b32_e32 v99, v195, v34, vcc
	v_cmp_lt_i32_e32 vcc, s0, v72
	s_movk_i32 s0, 0x5ff
	s_nop 0
	v_cndmask_b32_e32 v100, v195, v35, vcc
	v_cmp_lt_i32_e32 vcc, s0, v72
	s_movk_i32 s0, 0x60f
	v_max3_f32 v20, v20, v99, v100
	v_cndmask_b32_e32 v101, v195, v4, vcc
	v_cmp_lt_i32_e32 vcc, s0, v72
	s_movk_i32 s0, 0x61f
	s_nop 0
	v_cndmask_b32_e32 v102, v195, v5, vcc
	v_cmp_lt_i32_e32 vcc, s0, v72
	s_movk_i32 s0, 0x62f
	v_max3_f32 v4, v20, v101, v102
	v_cndmask_b32_e32 v103, v195, v6, vcc
	v_cmp_lt_i32_e32 vcc, s0, v72
	s_movk_i32 s0, 0x67f
	s_nop 0
	v_cndmask_b32_e32 v104, v195, v7, vcc
	v_cmp_lt_i32_e32 vcc, s0, v72
	s_movk_i32 s0, 0x68f
	v_max3_f32 v4, v4, v103, v104
	v_cndmask_b32_e32 v58, v195, v8, vcc
	v_cmp_lt_i32_e32 vcc, s0, v72
	s_movk_i32 s0, 0x69f
	s_nop 0
	v_cndmask_b32_e32 v59, v195, v9, vcc
	v_cmp_lt_i32_e32 vcc, s0, v72
	s_movk_i32 s0, 0x6af
	v_max3_f32 v4, v4, v58, v59
	v_cndmask_b32_e32 v56, v195, v10, vcc
	v_cmp_lt_i32_e32 vcc, s0, v72
	s_movk_i32 s0, 0x6ff
	s_nop 0
	v_cndmask_b32_e32 v57, v195, v11, vcc
	v_cmp_lt_i32_e32 vcc, s0, v72
	s_movk_i32 s0, 0x70f
	v_max3_f32 v4, v4, v56, v57
	v_cndmask_b32_e32 v62, v195, v12, vcc
	v_cmp_lt_i32_e32 vcc, s0, v72
	s_movk_i32 s0, 0x71f
	s_nop 0
	v_cndmask_b32_e32 v63, v195, v13, vcc
	v_cmp_lt_i32_e32 vcc, s0, v72
	s_movk_i32 s0, 0x72f
	v_max3_f32 v4, v4, v62, v63
	v_cndmask_b32_e32 v60, v195, v14, vcc
	v_cmp_lt_i32_e32 vcc, s0, v72
	s_movk_i32 s0, 0x77f
	s_nop 0
	v_cndmask_b32_e32 v61, v195, v15, vcc
	v_cmp_lt_i32_e32 vcc, s0, v72
	s_movk_i32 s0, 0x78f
	v_max3_f32 v4, v4, v60, v61
	v_cndmask_b32_e32 v69, v195, v16, vcc
	v_cmp_lt_i32_e32 vcc, s0, v72
	s_movk_i32 s0, 0x79f
	s_nop 0
	v_cndmask_b32_e32 v66, v195, v17, vcc
	v_cmp_lt_i32_e32 vcc, s0, v72
	s_movk_i32 s0, 0x7af
	v_max3_f32 v4, v4, v69, v66
	v_cndmask_b32_e32 v65, v195, v18, vcc
	v_cmp_lt_i32_e32 vcc, s0, v72
	s_mov_b32 s0, 0xefa18f08
	s_nop 0
	v_cndmask_b32_e32 v64, v195, v19, vcc
	v_max3_f32 v4, v4, v65, v64
	v_mov_b32_e32 v5, v4
	s_nop 1
	v_permlane32_swap_b32_e32 v4, v5
	v_max3_f32 v67, v4, v5, s0
	v_sub_f32_e32 v4, v52, v67
	v_exp_f32_e32 v4, v4
	v_sub_f32_e32 v5, v53, v67
	v_exp_f32_e32 v5, v5
	v_sub_f32_e32 v9, v73, v67
	v_add_f32_e32 v6, 0, v4
	v_exp_f32_e32 v10, v9
	v_add_f32_e32 v7, v5, v6
	v_sub_f32_e32 v6, v54, v67
	v_exp_f32_e32 v6, v6
	v_sub_f32_e32 v9, v74, v67
	v_exp_f32_e32 v11, v9
	v_sub_f32_e32 v13, v77, v67
	v_add_f32_e32 v8, v6, v7
	v_sub_f32_e32 v7, v55, v67
	v_exp_f32_e32 v7, v7
	v_exp_f32_e32 v14, v13
	v_sub_f32_e32 v13, v78, v67
	v_exp_f32_e32 v15, v13
	v_add_f32_e32 v8, v7, v8
	v_add_f32_e32 v8, v10, v8
	v_add_f32_e32 v9, v11, v8
	v_sub_f32_e32 v8, v75, v67
	v_exp_f32_e32 v8, v8
	v_sub_f32_e32 v17, v81, v67
	v_exp_f32_e32 v18, v17
	v_sub_f32_e32 v17, v82, v67
	v_add_f32_e32 v12, v8, v9
	v_sub_f32_e32 v9, v76, v67
	v_exp_f32_e32 v9, v9
	v_exp_f32_e32 v19, v17
	v_sub_f32_e32 v21, v36, v67
	v_exp_f32_e32 v22, v21
	v_add_f32_e32 v12, v9, v12
	v_add_f32_e32 v12, v14, v12
	v_add_f32_e32 v13, v15, v12
	v_sub_f32_e32 v12, v79, v67
	v_exp_f32_e32 v12, v12
	v_sub_f32_e32 v21, v37, v67
	v_exp_f32_e32 v23, v21
	v_sub_f32_e32 v25, v40, v67
	v_add_f32_e32 v16, v12, v13
	v_sub_f32_e32 v13, v80, v67
	v_exp_f32_e32 v13, v13
	v_exp_f32_e32 v26, v25
	v_sub_f32_e32 v25, v41, v67
	v_exp_f32_e32 v27, v25
	v_add_f32_e32 v16, v13, v16
	v_add_f32_e32 v16, v18, v16
	v_add_f32_e32 v17, v19, v16
	v_sub_f32_e32 v16, v83, v67
	v_exp_f32_e32 v16, v16
	v_sub_f32_e32 v29, v44, v67
	v_exp_f32_e32 v30, v29
	v_sub_f32_e32 v29, v45, v67
	v_add_f32_e32 v20, v16, v17
	v_sub_f32_e32 v17, v84, v67
	v_exp_f32_e32 v17, v17
	v_exp_f32_e32 v31, v29
	v_sub_f32_e32 v33, v48, v67
	v_exp_f32_e32 v34, v33
	v_add_f32_e32 v20, v17, v20
	v_add_f32_e32 v20, v22, v20
	v_add_f32_e32 v21, v23, v20
	v_sub_f32_e32 v20, v38, v67
	v_exp_f32_e32 v20, v20
	v_sub_f32_e32 v33, v49, v67
	v_exp_f32_e32 v35, v33
	v_sub_f32_e32 v37, v85, v67
	v_add_f32_e32 v24, v20, v21
	v_sub_f32_e32 v21, v39, v67
	v_exp_f32_e32 v21, v21
	v_exp_f32_e32 v38, v37
	v_sub_f32_e32 v37, v86, v67
	v_exp_f32_e32 v39, v37
	v_add_f32_e32 v24, v21, v24
	v_add_f32_e32 v24, v26, v24
	v_add_f32_e32 v25, v27, v24
	v_sub_f32_e32 v24, v42, v67
	v_exp_f32_e32 v24, v24
	v_sub_f32_e32 v41, v89, v67
	v_exp_f32_e32 v42, v41
	v_sub_f32_e32 v41, v90, v67
	v_add_f32_e32 v28, v24, v25
	v_sub_f32_e32 v25, v43, v67
	v_exp_f32_e32 v25, v25
	v_exp_f32_e32 v43, v41
	v_sub_f32_e32 v45, v93, v67
	v_sub_f32_e32 v49, v97, v67
	v_add_f32_e32 v28, v25, v28
	v_add_f32_e32 v28, v30, v28
	v_add_f32_e32 v29, v31, v28
	v_sub_f32_e32 v28, v46, v67
	v_exp_f32_e32 v28, v28
	v_exp_f32_e32 v46, v45
	v_sub_f32_e32 v45, v94, v67
	v_sub_f32_e32 v53, v101, v67
	v_add_f32_e32 v32, v28, v29
	v_sub_f32_e32 v29, v47, v67
	v_exp_f32_e32 v29, v29
	v_exp_f32_e32 v47, v45
	v_exp_f32_e32 v54, v53
	v_sub_f32_e32 v53, v102, v67
	v_add_f32_e32 v32, v29, v32
	v_add_f32_e32 v32, v34, v32
	v_add_f32_e32 v33, v35, v32
	v_sub_f32_e32 v32, v50, v67
	v_exp_f32_e32 v32, v32
	v_exp_f32_e32 v50, v49
	v_sub_f32_e32 v49, v98, v67
	v_exp_f32_e32 v55, v53
	v_add_f32_e32 v36, v32, v33
	v_sub_f32_e32 v33, v51, v67
	v_exp_f32_e32 v33, v33
	v_exp_f32_e32 v51, v49
	v_sub_f32_e32 v58, v58, v67
	v_exp_f32_e32 v58, v58
	v_add_f32_e32 v36, v33, v36
	v_add_f32_e32 v36, v38, v36
	v_add_f32_e32 v37, v39, v36
	v_sub_f32_e32 v36, v87, v67
	v_exp_f32_e32 v36, v36
	v_sub_f32_e32 v59, v59, v67
	v_exp_f32_e32 v59, v59
	v_sub_f32_e32 v56, v56, v67
	v_add_f32_e32 v40, v36, v37
	v_sub_f32_e32 v37, v88, v67
	v_exp_f32_e32 v37, v37
	v_exp_f32_e32 v56, v56
	v_sub_f32_e32 v57, v57, v67
	v_exp_f32_e32 v57, v57
	v_add_f32_e32 v40, v37, v40
	v_add_f32_e32 v40, v42, v40
	v_add_f32_e32 v41, v43, v40
	v_sub_f32_e32 v40, v91, v67
	v_exp_f32_e32 v40, v40
	v_sub_f32_e32 v62, v62, v67
	v_exp_f32_e32 v62, v62
	v_sub_f32_e32 v63, v63, v67
	v_add_f32_e32 v44, v40, v41
	v_sub_f32_e32 v41, v92, v67
	v_exp_f32_e32 v41, v41
	v_exp_f32_e32 v63, v63
	v_sub_f32_e32 v60, v60, v67
	v_exp_f32_e32 v60, v60
	v_add_f32_e32 v44, v41, v44
	v_add_f32_e32 v44, v46, v44
	v_add_f32_e32 v45, v47, v44
	v_sub_f32_e32 v44, v95, v67
	v_exp_f32_e32 v44, v44
	v_sub_f32_e32 v61, v61, v67
	v_exp_f32_e32 v61, v61
	v_sub_f32_e32 v69, v69, v67
	v_add_f32_e32 v48, v44, v45
	v_sub_f32_e32 v45, v96, v67
	v_exp_f32_e32 v45, v45
	v_sub_f32_e32 v66, v66, v67
	v_sub_f32_e32 v65, v65, v67
	v_sub_f32_e32 v64, v64, v67
	v_add_f32_e32 v48, v45, v48
	v_add_f32_e32 v48, v50, v48
	v_add_f32_e32 v49, v51, v48
	v_sub_f32_e32 v48, v99, v67
	v_exp_f32_e32 v48, v48
	s_nop 0
	v_add_f32_e32 v52, v48, v49
	v_sub_f32_e32 v49, v100, v67
	v_exp_f32_e32 v49, v49
	s_nop 0
	v_add_f32_e32 v52, v49, v52
	v_add_f32_e32 v52, v54, v52
	v_add_f32_e32 v53, v55, v52
	v_sub_f32_e32 v52, v103, v67
	v_exp_f32_e32 v52, v52
	s_nop 0
	v_add_f32_e32 v72, v52, v53
	v_sub_f32_e32 v53, v104, v67
	v_exp_f32_e32 v53, v53
	v_exp_f32_e32 v67, v64
	v_add_f32_e32 v72, v53, v72
	v_add_f32_e32 v72, v58, v72
	v_add_f32_e32 v72, v59, v72
	v_add_f32_e32 v72, v56, v72
	v_add_f32_e32 v72, v57, v72
	v_add_f32_e32 v72, v62, v72
	v_add_f32_e32 v72, v63, v72
	v_add_f32_e32 v72, v60, v72
	v_add_f32_e32 v73, v61, v72
	v_exp_f32_e32 v72, v69
	s_nop 0
	v_add_f32_e32 v69, v72, v73
	v_exp_f32_e32 v73, v66
	v_exp_f32_e32 v66, v65
	v_add_f32_e32 v69, v73, v69
	v_add_f32_e32 v65, v66, v69
	v_add_f32_e32 v64, v67, v65
	v_mov_b32_e32 v65, v64
	s_nop 1
	v_permlane32_swap_b32_e32 v64, v65
	v_add_f32_e32 v64, v64, v65
	v_div_scale_f32 v65, s[2:3], v64, v64, 1.0
	v_rcp_f32_e32 v69, v65
	v_cmp_lt_f32_e64 s[0:1], 0, v64
	v_fma_f32 v74, -v65, v69, 1.0
	v_fmac_f32_e32 v69, v74, v69
	v_div_scale_f32 v74, vcc, 1.0, v64, 1.0
	v_mul_f32_e32 v75, v74, v69
	v_fma_f32 v76, -v65, v75, v74
	v_fmac_f32_e32 v75, v76, v69
	v_fma_f32 v65, -v65, v75, v74
	v_div_fmas_f32 v65, v65, v69, v75
	v_and_b32_e32 v69, 64, v212
	v_div_fixup_f32 v64, v65, v64, 1.0
	v_xor_b32_e32 v65, 32, v212
	v_add_u32_e32 v69, 64, v69
	v_cmp_lt_i32_e32 vcc, v65, v69
	v_cndmask_b32_e64 v76, 0, v64, s[0:1]
	v_add_u32_e32 v64, s12, v71
	v_cndmask_b32_e32 v65, v212, v65, vcc
	v_lshlrev_b32_e32 v77, 2, v65
	v_pk_mul_f32 v[6:7], v[6:7], v[76:77] op_sel_hi:[1,0]
	ds_bpermute_b32 v74, v77, v7
	v_mul_lo_u32 v64, v64, s64
	v_lshlrev_b32_e32 v69, 2, v3
	v_add3_u32 v88, s33, v64, v69
	v_pk_mul_f32 v[64:65], v[4:5], v[76:77] op_sel_hi:[1,0]
	v_cmp_gt_u32_e32 vcc, 32, v68
	v_pk_mul_f32 v[4:5], v[70:71], v[64:65] op_sel_hi:[0,1]
	v_add_f32_e32 v75, v6, v7
	v_add_f32_e32 v64, v64, v65
	v_add_f32_e32 v64, v64, v75
	s_waitcnt lgkmcnt(0)
	v_cndmask_b32_e64 v65, v74, 0, vcc
	v_pk_mul_f32 v[8:9], v[8:9], v[76:77] op_sel_hi:[1,0]
	v_add_f32_e32 v64, v65, v64
	ds_bpermute_b32 v65, v77, v9
	v_pk_mul_f32 v[10:11], v[10:11], v[76:77] op_sel_hi:[1,0]
	v_add_f32_e32 v75, v8, v9
	v_pk_mul_f32 v[78:79], v[70:71], v[10:11] op_sel_hi:[0,1]
	v_add_f32_e32 v10, v10, v11
	v_add_f32_e32 v10, v10, v75
	s_waitcnt lgkmcnt(0)
	v_cndmask_b32_e32 v11, v65, v74, vcc
	v_add_f32_e32 v10, v11, v10
	ds_write2_b32 v88, v64, v10 offset1:2
	v_pk_mul_f32 v[10:11], v[12:13], v[76:77] op_sel_hi:[1,0]
	ds_bpermute_b32 v12, v77, v11
	v_add_f32_e32 v13, v10, v11
	v_pk_mul_f32 v[84:85], v[70:71], v[10:11] op_sel_hi:[0,1]
	v_pk_mul_f32 v[10:11], v[16:17], v[76:77] op_sel_hi:[1,0]
	v_pk_mul_f32 v[80:81], v[70:71], v[8:9] op_sel_hi:[0,1]
	v_pk_mul_f32 v[8:9], v[14:15], v[76:77] op_sel_hi:[1,0]
	ds_bpermute_b32 v14, v77, v11
	v_pk_mul_f32 v[82:83], v[70:71], v[8:9] op_sel_hi:[0,1]
	v_add_f32_e32 v8, v8, v9
	v_add_f32_e32 v8, v8, v13
	s_waitcnt lgkmcnt(1)
	v_cndmask_b32_e32 v9, v12, v65, vcc
	v_add_f32_e32 v13, v9, v8
	v_pk_mul_f32 v[8:9], v[18:19], v[76:77] op_sel_hi:[1,0]
	v_add_f32_e32 v15, v10, v11
	v_pk_mul_f32 v[86:87], v[70:71], v[10:11] op_sel_hi:[0,1]
	v_pk_mul_f32 v[10:11], v[20:21], v[76:77] op_sel_hi:[1,0]
	v_pk_mul_f32 v[18:19], v[70:71], v[8:9] op_sel_hi:[0,1]
	v_add_f32_e32 v8, v8, v9
	s_waitcnt lgkmcnt(0)
	v_cndmask_b32_e32 v9, v14, v12, vcc
	ds_bpermute_b32 v12, v77, v11
	v_add_f32_e32 v8, v8, v15
	v_add_f32_e32 v8, v9, v8
	ds_write2_b32 v88, v13, v8 offset0:4 offset1:6
	v_pk_mul_f32 v[8:9], v[22:23], v[76:77] op_sel_hi:[1,0]
	v_add_f32_e32 v13, v10, v11
	v_pk_mul_f32 v[20:21], v[70:71], v[10:11] op_sel_hi:[0,1]
	v_pk_mul_f32 v[10:11], v[24:25], v[76:77] op_sel_hi:[1,0]
	v_pk_mul_f32 v[22:23], v[70:71], v[8:9] op_sel_hi:[0,1]
	v_add_f32_e32 v8, v8, v9
	s_waitcnt lgkmcnt(1)
	v_cndmask_b32_e32 v9, v12, v14, vcc
	ds_bpermute_b32 v14, v77, v11
	v_add_f32_e32 v8, v8, v13
	v_add_f32_e32 v13, v8, v9
	v_pk_mul_f32 v[8:9], v[26:27], v[76:77] op_sel_hi:[1,0]
	v_add_f32_e32 v15, v10, v11
	v_pk_mul_f32 v[24:25], v[70:71], v[10:11] op_sel_hi:[0,1]
	v_pk_mul_f32 v[10:11], v[28:29], v[76:77] op_sel_hi:[1,0]
	v_pk_mul_f32 v[26:27], v[70:71], v[8:9] op_sel_hi:[0,1]
	v_add_f32_e32 v8, v8, v9
	s_waitcnt lgkmcnt(0)
	v_cndmask_b32_e32 v9, v14, v12, vcc
	ds_bpermute_b32 v12, v77, v11
	v_add_f32_e32 v8, v8, v15
	v_add_f32_e32 v8, v8, v9
	ds_write2_b32 v88, v13, v8 offset0:8 offset1:10
	v_pk_mul_f32 v[8:9], v[30:31], v[76:77] op_sel_hi:[1,0]
	v_add_f32_e32 v13, v10, v11
	v_pk_mul_f32 v[28:29], v[70:71], v[10:11] op_sel_hi:[0,1]
	v_pk_mul_f32 v[10:11], v[32:33], v[76:77] op_sel_hi:[1,0]
	v_pk_mul_f32 v[30:31], v[70:71], v[8:9] op_sel_hi:[0,1]
	v_add_f32_e32 v8, v8, v9
	s_waitcnt lgkmcnt(1)
	v_cndmask_b32_e32 v9, v12, v14, vcc
	ds_bpermute_b32 v14, v77, v11
	v_add_f32_e32 v8, v8, v13
	v_add_f32_e32 v13, v8, v9
	v_pk_mul_f32 v[8:9], v[34:35], v[76:77] op_sel_hi:[1,0]
	v_add_f32_e32 v15, v10, v11
	v_pk_mul_f32 v[34:35], v[70:71], v[8:9] op_sel_hi:[0,1]
	v_add_f32_e32 v8, v8, v9
	v_add_f32_e32 v8, v8, v15
	s_waitcnt lgkmcnt(0)
	v_cndmask_b32_e32 v9, v14, v12, vcc
	v_add_f32_e32 v8, v8, v9
	ds_write2_b32 v88, v13, v8 offset0:12 offset1:14
	v_pk_mul_f32 v[12:13], v[36:37], v[76:77] op_sel_hi:[1,0]
	ds_bpermute_b32 v36, v77, v13
	v_pk_mul_f32 v[16:17], v[40:41], v[76:77] op_sel_hi:[1,0]
	ds_bpermute_b32 v40, v77, v17
	v_pk_mul_f32 v[32:33], v[70:71], v[10:11] op_sel_hi:[0,1]
	v_pk_mul_f32 v[10:11], v[38:39], v[76:77] op_sel_hi:[1,0]
	v_add_f32_e32 v15, v12, v13
	v_pk_mul_f32 v[8:9], v[70:71], v[10:11] op_sel_hi:[0,1]
	v_add_f32_e32 v10, v10, v11
	v_add_f32_e32 v10, v10, v15
	s_waitcnt lgkmcnt(1)
	v_cndmask_b32_e32 v11, v36, v14, vcc
	v_pk_mul_f32 v[14:15], v[42:43], v[76:77] op_sel_hi:[1,0]
	v_add_f32_e32 v37, v10, v11
	v_pk_mul_f32 v[10:11], v[70:71], v[12:13] op_sel_hi:[0,1]
	v_pk_mul_f32 v[12:13], v[70:71], v[14:15] op_sel_hi:[0,1]
	v_add_f32_e32 v38, v16, v17
	v_add_f32_e32 v14, v14, v15
	v_add_f32_e32 v14, v14, v38
	s_waitcnt lgkmcnt(0)
	v_cndmask_b32_e32 v15, v40, v36, vcc
	v_pk_mul_f32 v[38:39], v[44:45], v[76:77] op_sel_hi:[1,0]
	v_add_f32_e32 v14, v14, v15
	ds_bpermute_b32 v41, v77, v39
	ds_write2_b32 v88, v37, v14 offset0:16 offset1:18
	v_pk_mul_f32 v[36:37], v[46:47], v[76:77] op_sel_hi:[1,0]
	v_pk_mul_f32 v[14:15], v[70:71], v[16:17] op_sel_hi:[0,1]
	v_pk_mul_f32 v[16:17], v[70:71], v[36:37] op_sel_hi:[0,1]
	v_add_f32_e32 v42, v38, v39
	v_add_f32_e32 v36, v36, v37
	v_pk_mul_f32 v[64:65], v[70:71], v[38:39] op_sel_hi:[0,1]
	v_pk_mul_f32 v[38:39], v[48:49], v[76:77] op_sel_hi:[1,0]
	v_add_f32_e32 v36, v36, v42
	ds_bpermute_b32 v42, v77, v39
	s_waitcnt lgkmcnt(2)
	v_cndmask_b32_e32 v37, v41, v40, vcc
	v_add_f32_e32 v40, v36, v37
	v_pk_mul_f32 v[36:37], v[50:51], v[76:77] op_sel_hi:[1,0]
	v_add_f32_e32 v43, v38, v39
	v_pk_mul_f32 v[50:51], v[70:71], v[36:37] op_sel_hi:[0,1]
	v_add_f32_e32 v36, v36, v37
	v_add_f32_e32 v36, v36, v43
	s_waitcnt lgkmcnt(0)
	v_cndmask_b32_e32 v37, v42, v41, vcc
	v_add_f32_e32 v36, v36, v37
	v_pk_mul_f32 v[74:75], v[70:71], v[38:39] op_sel_hi:[0,1]
	v_pk_mul_f32 v[38:39], v[52:53], v[76:77] op_sel_hi:[1,0]
	ds_write2_b32 v88, v40, v36 offset0:20 offset1:22
	ds_bpermute_b32 v40, v77, v39
	v_pk_mul_f32 v[36:37], v[54:55], v[76:77] op_sel_hi:[1,0]
	v_add_f32_e32 v41, v38, v39
	v_pk_mul_f32 v[52:53], v[70:71], v[38:39] op_sel_hi:[0,1]
	v_pk_mul_f32 v[38:39], v[56:57], v[76:77] op_sel_hi:[1,0]
	v_pk_mul_f32 v[54:55], v[70:71], v[36:37] op_sel_hi:[0,1]
	v_add_f32_e32 v36, v36, v37
	s_waitcnt lgkmcnt(0)
	v_cndmask_b32_e32 v37, v40, v42, vcc
	ds_bpermute_b32 v42, v77, v39
	v_add_f32_e32 v36, v36, v41
	v_add_f32_e32 v41, v36, v37
	v_pk_mul_f32 v[36:37], v[58:59], v[76:77] op_sel_hi:[1,0]
	v_add_f32_e32 v43, v38, v39
	v_pk_mul_f32 v[56:57], v[70:71], v[38:39] op_sel_hi:[0,1]
	v_pk_mul_f32 v[38:39], v[60:61], v[76:77] op_sel_hi:[1,0]
	v_pk_mul_f32 v[58:59], v[70:71], v[36:37] op_sel_hi:[0,1]
	v_add_f32_e32 v36, v36, v37
	s_waitcnt lgkmcnt(0)
	v_cndmask_b32_e32 v37, v42, v40, vcc
	ds_bpermute_b32 v40, v77, v39
	v_add_f32_e32 v36, v36, v43
	v_add_f32_e32 v36, v36, v37
	ds_write2_b32 v88, v41, v36 offset0:24 offset1:26
	v_pk_mul_f32 v[36:37], v[62:63], v[76:77] op_sel_hi:[1,0]
	v_add_f32_e32 v41, v38, v39
	v_pk_mul_f32 v[60:61], v[70:71], v[38:39] op_sel_hi:[0,1]
	v_pk_mul_f32 v[38:39], v[66:67], v[76:77] op_sel_hi:[1,0]
	v_pk_mul_f32 v[62:63], v[70:71], v[36:37] op_sel_hi:[0,1]
	v_add_f32_e32 v36, v36, v37
	s_waitcnt lgkmcnt(1)
	v_cndmask_b32_e32 v37, v40, v42, vcc
	ds_bpermute_b32 v42, v77, v39
	v_add_f32_e32 v36, v36, v41
	v_add_f32_e32 v41, v36, v37
	v_pk_mul_f32 v[36:37], v[72:73], v[76:77] op_sel_hi:[1,0]
	v_add_f32_e32 v43, v38, v39
	v_pk_mul_f32 v[72:73], v[70:71], v[36:37] op_sel_hi:[0,1]
	v_add_f32_e32 v36, v36, v37
	v_cvt_pk_bf16_f32 v78, v78, v79
	v_cvt_pk_bf16_f32 v79, v80, v81
	v_cvt_pk_bf16_f32 v80, v82, v83
	v_cvt_pk_bf16_f32 v82, v18, v19
	v_lshlrev_b32_e32 v18, 1, v68
	v_bfe_u32 v19, v68, 2, 2
	s_mov_b32 s0, 0x3fffffc
	v_add_f32_e32 v36, v36, v43
	s_waitcnt lgkmcnt(0)
	v_cndmask_b32_e32 v37, v42, v40, vcc
	v_and_b32_e32 v204, 32, v18
	v_and_or_b32 v19, v182, s0, v19
	v_add_f32_e32 v36, v36, v37
	v_add_u32_e32 v18, 0, v204
	v_lshlrev_b32_e32 v205, 6, v19
	v_pk_mul_f32 v[6:7], v[70:71], v[6:7] op_sel_hi:[0,1]
	ds_write2_b32 v88, v41, v36 offset0:28 offset1:30
	v_pk_mul_f32 v[66:67], v[70:71], v[38:39] op_sel_hi:[0,1]
	v_add3_u32 v70, v18, v201, v205
	v_add3_u32 v229, v18, v201, v205
	v_cvt_pk_bf16_f32 v81, v84, v85
	v_cvt_pk_bf16_f32 v83, v86, v87
	v_cvt_pk_bf16_f32 v84, v22, v23
	v_cvt_pk_bf16_f32 v85, v20, v21
	v_cvt_pk_bf16_f32 v87, v24, v25
	ds_read_b64_tr_b16 v[18:19], v70 offset:8192
	ds_read_b64_tr_b16 v[20:21], v70 offset:8704
	ds_read_b64_tr_b16 v[22:23], v70 offset:12288
	ds_read_b64_tr_b16 v[24:25], v70 offset:12800
	v_cvt_pk_bf16_f32 v76, v4, v5
	v_cvt_pk_bf16_f32 v77, v6, v7
	v_cvt_pk_bf16_f32 v86, v26, v27
	v_cvt_pk_bf16_f32 v4, v30, v31
	v_cvt_pk_bf16_f32 v5, v28, v29
	v_cvt_pk_bf16_f32 v6, v34, v35
	v_cvt_pk_bf16_f32 v7, v32, v33
	s_waitcnt lgkmcnt(2)
	v_mfma_f32_32x32x16_bf16 v[34:49], v[18:21], v[76:79], 0
	s_waitcnt lgkmcnt(0)
	v_mfma_f32_32x32x16_bf16 v[18:33], v[22:25], v[76:79], 0
	ds_read_b64_tr_b16 v[76:77], v70 offset:9216
	ds_read_b64_tr_b16 v[78:79], v70 offset:9728
	ds_read_b64_tr_b16 v[88:89], v70 offset:13312
	ds_read_b64_tr_b16 v[90:91], v70 offset:13824
	s_waitcnt lgkmcnt(2)
	v_mfma_f32_32x32x16_bf16 v[34:49], v[76:79], v[80:83], v[34:49]
	s_waitcnt lgkmcnt(0)
	v_mfma_f32_32x32x16_bf16 v[18:33], v[88:91], v[80:83], v[18:33]
	ds_read_b64_tr_b16 v[76:77], v70 offset:10240
	ds_read_b64_tr_b16 v[78:79], v70 offset:10752
	ds_read_b64_tr_b16 v[80:81], v70 offset:14336
	ds_read_b64_tr_b16 v[82:83], v70 offset:14848
	s_waitcnt lgkmcnt(2)
	v_mfma_f32_32x32x16_bf16 v[34:49], v[76:79], v[84:87], v[34:49]
	s_waitcnt lgkmcnt(0)
	v_mfma_f32_32x32x16_bf16 v[18:33], v[80:83], v[84:87], v[18:33]
	ds_read_b64_tr_b16 v[76:77], v70 offset:11264
	ds_read_b64_tr_b16 v[78:79], v70 offset:11776
	ds_read_b64_tr_b16 v[80:81], v70 offset:15360
	ds_read_b64_tr_b16 v[82:83], v70 offset:15872
	s_waitcnt lgkmcnt(2)
	v_mfma_f32_32x32x16_bf16 v[34:49], v[76:79], v[4:7], v[34:49]
	v_cvt_pk_bf16_f32 v76, v8, v9
	v_cvt_pk_bf16_f32 v77, v10, v11
	v_cvt_pk_bf16_f32 v79, v14, v15
	v_cvt_pk_bf16_f32 v14, v50, v51
	v_cvt_pk_bf16_f32 v8, v54, v55
	v_cvt_pk_bf16_f32 v9, v52, v53
	v_cvt_pk_bf16_f32 v11, v56, v57
	s_waitcnt lgkmcnt(0)
	v_mfma_f32_32x32x16_bf16 v[18:33], v[80:83], v[4:7], v[18:33]
	ds_read_b64_tr_b16 v[50:51], v70 offset:24576
	ds_read_b64_tr_b16 v[52:53], v70 offset:25088
	ds_read_b64_tr_b16 v[54:55], v70 offset:28672
	ds_read_b64_tr_b16 v[56:57], v70 offset:29184
	v_cvt_pk_bf16_f32 v78, v12, v13
	v_cvt_pk_bf16_f32 v12, v16, v17
	v_cvt_pk_bf16_f32 v13, v64, v65
	v_cvt_pk_bf16_f32 v15, v74, v75
	v_cvt_pk_bf16_f32 v10, v58, v59
	v_cvt_pk_bf16_f32 v4, v62, v63
	s_waitcnt lgkmcnt(2)
	v_mfma_f32_32x32x16_bf16 v[34:49], v[50:53], v[76:79], v[34:49]
	v_cvt_pk_bf16_f32 v5, v60, v61
	v_cvt_pk_bf16_f32 v6, v72, v73
	v_cvt_pk_bf16_f32 v7, v66, v67
	s_waitcnt lgkmcnt(0)
	v_mfma_f32_32x32x16_bf16 v[18:33], v[54:57], v[76:79], v[18:33]
	ds_read_b64_tr_b16 v[50:51], v70 offset:25600
	ds_read_b64_tr_b16 v[52:53], v70 offset:26112
	ds_read_b64_tr_b16 v[54:55], v70 offset:29696
	ds_read_b64_tr_b16 v[56:57], v70 offset:30208
	s_waitcnt lgkmcnt(2)
	v_mfma_f32_32x32x16_bf16 v[34:49], v[50:53], v[12:15], v[34:49]
	s_waitcnt lgkmcnt(0)
	v_mfma_f32_32x32x16_bf16 v[18:33], v[54:57], v[12:15], v[18:33]
	ds_read_b64_tr_b16 v[12:13], v70 offset:26624
	ds_read_b64_tr_b16 v[14:15], v70 offset:27136
	ds_read_b64_tr_b16 v[50:51], v70 offset:30720
	ds_read_b64_tr_b16 v[52:53], v70 offset:31232
	s_waitcnt lgkmcnt(2)
	v_mfma_f32_32x32x16_bf16 v[34:49], v[12:15], v[8:11], v[34:49]
	s_waitcnt lgkmcnt(0)
	v_mfma_f32_32x32x16_bf16 v[18:33], v[50:53], v[8:11], v[18:33]
	ds_read_b64_tr_b16 v[8:9], v70 offset:27648
	ds_read_b64_tr_b16 v[10:11], v70 offset:28160
	ds_read_b64_tr_b16 v[12:13], v70 offset:31744
	ds_read_b64_tr_b16 v[14:15], v70 offset:32256
	s_waitcnt lgkmcnt(2)
	v_mfma_f32_32x32x16_bf16 v[34:49], v[8:11], v[4:7], v[34:49]
	s_waitcnt lgkmcnt(0)
	v_mfma_f32_32x32x16_bf16 v[18:33], v[12:15], v[4:7], v[18:33]
	s_cbranch_scc1 .LBB0_640
	s_cmp_gt_u32 s78, 7
	s_cselect_b64 s[94:95], -1, 0
	s_cmp_gt_u32 s82, 3
	s_cselect_b64 s[96:97], -1, 0
	s_sub_i32 s0, 3, s80
	s_mov_b32 s1, s16
	s_lshl_b64 s[0:1], s[0:1], 13
	v_readlane_b32 s9, v251, 59
	s_add_u32 s2, s9, s0
	v_readlane_b32 s10, v251, 61
	s_addc_u32 s3, s10, s1
	s_add_i32 s0, s79, 4
	s_mov_b32 s1, s16
	s_lshl_b64 s[0:1], s[0:1], 13
	v_writelane_b32 v249, s40, 10
	s_add_u32 s7, s92, s0
	s_mov_b32 s12, s16
	s_addc_u32 s8, s93, s1
	s_mov_b32 s1, s16
	v_writelane_b32 v249, s12, 11
	s_cmp_gt_u32 s82, 4
	s_cselect_b64 s[4:5], -1, 0
	v_writelane_b32 v249, s13, 12
	s_sub_i32 s0, 4, s80
	v_writelane_b32 v249, s14, 13
	s_lshl_b64 s[0:1], s[0:1], 13
	v_writelane_b32 v249, s15, 14
	s_add_u32 s9, s9, s0
	v_writelane_b32 v249, s16, 15
	s_addc_u32 s10, s10, s1
	s_add_i32 s0, s79, 5
	v_writelane_b32 v249, s17, 16
	s_mov_b32 s1, s16
	v_writelane_b32 v249, s18, 17
	s_lshl_b64 s[0:1], s[0:1], 13
	v_writelane_b32 v249, s19, 18
	s_add_u32 s0, s92, s0
	v_writelane_b32 v249, s20, 19
	s_addc_u32 s1, s93, s1
	s_sub_i32 s11, 30, s6
	v_writelane_b32 v249, s21, 20
	s_cmp_gt_i32 s80, 3
	v_writelane_b32 v249, s22, 21
	s_cselect_b32 s2, s7, s2
	v_writelane_b32 v249, s23, 22
	s_cselect_b32 s3, s8, s3
	s_add_u32 s2, s2, s90
	v_writelane_b32 v249, s24, 23
	s_addc_u32 s3, s3, s91
	v_writelane_b32 v249, s25, 24
	s_cmp_gt_i32 s80, 4
	v_writelane_b32 v249, s26, 25
	s_cselect_b32 s0, s0, s9
	v_writelane_b32 v249, s27, 26
	s_cselect_b32 s1, s1, s10
	s_add_u32 s12, s0, s90
	s_addc_u32 s13, s1, s91
	v_cmp_eq_u32_e32 vcc, 0, v198
	v_cmp_eq_u32_e64 s[0:1], s78, v198
	s_or_b64 s[0:1], vcc, s[0:1]
	v_cmp_eq_u32_e32 vcc, s11, v198
	s_or_b64 s[8:9], s[0:1], vcc
	v_readlane_b32 s0, v250, 44
	v_and_b32_e32 v4, 0x3fffffe0, v68
	v_lshl_add_u64 v[186:187], s[2:3], 0, v[184:185]
	v_lshl_add_u32 v206, v68, 2, s0
	v_lshl_add_u32 v207, v4, 2, s0
	s_mov_b64 s[0:1], 0x800000
	v_lshl_add_u64 v[190:191], s[12:13], 0, v[184:185]
	v_sub_u32_e32 v208, v71, v69
	v_lshl_add_u64 v[188:189], v[186:187], 0, s[0:1]
	v_lshl_add_u64 v[192:193], v[190:191], 0, s[0:1]
	v_mul_lo_u32 v3, v3, s64
	v_lshlrev_b32_e32 v4, 2, v198
	v_readlane_b32 s0, v250, 47
	v_lshlrev_b32_e32 v50, 2, v71
	v_mov_b32_e32 v16, v2
	v_add3_u32 v209, s0, v3, v4
	v_cmp_gt_i32_e64 s[0:1], 1, v208
	v_mov_b32_e32 v17, v2
	s_sub_i32 s83, s80, s6
	v_writelane_b32 v249, s0, 27
	v_mov_b32_e32 v3, v2
	v_mov_b32_e32 v4, v2
	v_writelane_b32 v249, s1, 28
	v_cmp_gt_i32_e64 s[0:1], 0, v208
	v_mov_b32_e32 v5, v2
	v_mov_b32_e32 v6, v2
	v_writelane_b32 v249, s0, 29
	v_mov_b32_e32 v7, v2
	v_mov_b32_e32 v8, v2
	v_writelane_b32 v249, s1, 30
	v_cmp_gt_i32_e64 s[0:1], 33, v208
	v_mov_b32_e32 v9, v2
	v_mov_b32_e32 v10, v2
	v_writelane_b32 v249, s0, 31
	v_mov_b32_e32 v11, v2
	v_mov_b32_e32 v12, v2
	v_writelane_b32 v249, s1, 32
	v_cmp_gt_i32_e64 s[0:1], 32, v208
	v_mov_b32_e32 v13, v2
	v_mov_b32_e32 v14, v2
	v_writelane_b32 v249, s0, 33
	v_mov_b32_e32 v15, v2
	v_add_u32_e32 v50, 0, v50
	v_writelane_b32 v249, s1, 34
	v_cmp_gt_i32_e64 s[0:1], 3, v208
	v_mov_b64_e32 v[96:97], v[16:17]
	v_mov_b64_e32 v[112:113], v[16:17]
	v_writelane_b32 v249, s0, 35
	s_add_i32 s83, s83, 32
	v_cmp_lt_u32_e64 s[6:7], s78, v198
	v_writelane_b32 v249, s1, 36
	v_cmp_gt_i32_e64 s[0:1], 2, v208
	v_mov_b32_e32 v211, 0
	v_cmp_eq_u32_e64 s[10:11], 0, v68
	v_writelane_b32 v249, s0, 37
	v_cmp_ne_u32_e64 s[12:13], 0, v198
	v_cmp_lt_u32_e64 s[14:15], 1, v198
	v_writelane_b32 v249, s1, 38
	v_cmp_gt_i32_e64 s[0:1], 35, v208
	v_cmp_lt_u32_e64 s[16:17], 2, v198
	v_cmp_lt_u32_e64 s[18:19], 3, v198
	v_writelane_b32 v249, s0, 39
	v_cmp_lt_u32_e64 s[20:21], 4, v198
	v_cmp_lt_u32_e64 s[22:23], 5, v198
	v_writelane_b32 v249, s1, 40
	v_cmp_gt_i32_e64 s[0:1], 34, v208
	v_cmp_lt_u32_e64 s[24:25], 6, v198
	v_cmp_lt_u32_e64 s[26:27], 7, v198
	v_writelane_b32 v249, s0, 41
	v_cmp_lt_u32_e64 s[28:29], 8, v198
	v_cmp_lt_u32_e64 s[30:31], 9, v198
	v_writelane_b32 v249, s1, 42
	v_cmp_gt_i32_e64 s[0:1], 9, v208
	v_cmp_lt_u32_e64 s[34:35], 10, v198
	v_cmp_lt_u32_e64 s[36:37], 11, v198
	v_writelane_b32 v249, s0, 43
	v_cmp_lt_u32_e64 s[38:39], 12, v198
	v_cmp_lt_u32_e64 s[40:41], 13, v198
	v_writelane_b32 v249, s1, 44
	v_cmp_gt_i32_e64 s[0:1], 8, v208
	v_cmp_lt_u32_e64 s[42:43], 14, v198
	v_cmp_lt_u32_e64 s[44:45], 15, v198
	v_writelane_b32 v249, s0, 45
	v_cmp_lt_u32_e64 s[46:47], 16, v198
	v_cmp_lt_u32_e64 s[48:49], 17, v198
	v_writelane_b32 v249, s1, 46
	v_cmp_gt_i32_e64 s[0:1], 41, v208
	v_cmp_lt_u32_e64 s[50:51], 18, v198
	v_cmp_lt_u32_e64 s[52:53], 19, v198
	v_writelane_b32 v249, s0, 47
	v_cmp_lt_u32_e64 s[54:55], 20, v198
	v_cmp_lt_u32_e64 s[56:57], 21, v198
	v_writelane_b32 v249, s1, 48
	v_cmp_gt_i32_e64 s[0:1], 40, v208
	v_cmp_lt_u32_e64 s[58:59], 22, v198
	v_cmp_lt_u32_e64 s[60:61], 23, v198
	v_writelane_b32 v249, s0, 49
	v_cmp_lt_u32_e64 s[62:63], 24, v198
	s_mov_b32 s2, 0
	v_writelane_b32 v249, s1, 50
	v_cmp_gt_i32_e64 s[0:1], 11, v208
	v_mov_b32_e32 v214, 0
	v_add_u32_e32 v210, 0x20400, v50
	v_writelane_b32 v249, s0, 51
	v_mov_b32_e32 v114, 0
	v_mov_b64_e32 v[94:95], v[14:15]
	v_writelane_b32 v249, s1, 52
	v_cmp_gt_i32_e64 s[0:1], 10, v208
	v_mov_b64_e32 v[92:93], v[12:13]
	v_mov_b64_e32 v[90:91], v[10:11]
	v_writelane_b32 v249, s0, 53
	v_mov_b64_e32 v[88:89], v[8:9]
	v_mov_b64_e32 v[86:87], v[6:7]
	v_writelane_b32 v249, s1, 54
	v_cmp_gt_i32_e64 s[0:1], 43, v208
	v_mov_b64_e32 v[84:85], v[4:5]
	v_mov_b64_e32 v[82:83], v[2:3]
	v_writelane_b32 v249, s0, 55
	v_mov_b64_e32 v[110:111], v[14:15]
	v_mov_b64_e32 v[108:109], v[12:13]
	v_writelane_b32 v249, s1, 56
	v_cmp_gt_i32_e64 s[0:1], 42, v208
	v_mov_b64_e32 v[106:107], v[10:11]
	v_mov_b64_e32 v[104:105], v[8:9]
	v_writelane_b32 v249, s0, 57
	v_mov_b64_e32 v[102:103], v[6:7]
	v_mov_b64_e32 v[100:101], v[4:5]
	v_writelane_b32 v249, s1, 58
	v_cmp_gt_i32_e64 s[0:1], 17, v208
	v_mov_b64_e32 v[98:99], v[2:3]
	v_cmp_lt_u32_e64 s[64:65], 25, v198
	v_writelane_b32 v249, s0, 59
	v_cmp_lt_u32_e64 s[66:67], 26, v198
	v_cmp_lt_u32_e64 s[68:69], 27, v198
	v_writelane_b32 v249, s1, 60
	v_cmp_gt_i32_e64 s[0:1], 16, v208
	v_cmp_lt_u32_e64 s[70:71], 28, v198
	v_cmp_lt_u32_e64 s[72:73], 29, v198
	v_writelane_b32 v249, s0, 61
	v_cmp_eq_u32_e64 s[74:75], 31, v198
	s_nop 0
	v_writelane_b32 v249, s1, 62
	v_cmp_gt_i32_e64 s[0:1], 49, v208
	s_nop 1
	v_writelane_b32 v249, s0, 63
	s_nop 1
	v_writelane_b32 v248, s1, 0
	v_cmp_gt_i32_e64 s[0:1], 48, v208
	s_nop 1
	v_writelane_b32 v248, s0, 1
	s_nop 1
	v_writelane_b32 v248, s1, 2
	v_cmp_gt_i32_e64 s[0:1], 19, v208
	s_nop 1
	v_writelane_b32 v248, s0, 3
	s_nop 1
	v_writelane_b32 v248, s1, 4
	v_cmp_gt_i32_e64 s[0:1], 18, v208
	s_nop 1
	v_writelane_b32 v248, s0, 5
	s_nop 1
	v_writelane_b32 v248, s1, 6
	v_cmp_gt_i32_e64 s[0:1], 51, v208
	s_nop 1
	v_writelane_b32 v248, s0, 7
	s_nop 1
	v_writelane_b32 v248, s1, 8
	v_cmp_gt_i32_e64 s[0:1], 50, v208
	s_nop 1
	v_writelane_b32 v248, s0, 9
	s_nop 1
	v_writelane_b32 v248, s1, 10
	v_cmp_gt_i32_e64 s[0:1], 25, v208
	s_nop 1
	v_writelane_b32 v248, s0, 11
	s_nop 1
	v_writelane_b32 v248, s1, 12
	v_cmp_gt_i32_e64 s[0:1], 24, v208
	s_nop 1
	v_writelane_b32 v248, s0, 13
	s_nop 1
	v_writelane_b32 v248, s1, 14
	v_cmp_gt_i32_e64 s[0:1], 57, v208
	s_nop 1
	v_writelane_b32 v248, s0, 15
	s_nop 1
	v_writelane_b32 v248, s1, 16
	v_cmp_gt_i32_e64 s[0:1], 56, v208
	s_nop 1
	v_writelane_b32 v248, s0, 17
	s_nop 1
	v_writelane_b32 v248, s1, 18
	v_cmp_gt_i32_e64 s[0:1], 27, v208
	s_nop 1
	v_writelane_b32 v248, s0, 19
	s_nop 1
	v_writelane_b32 v248, s1, 20
	v_cmp_gt_i32_e64 s[0:1], 26, v208
	s_nop 1
	v_writelane_b32 v248, s0, 21
	s_nop 1
	v_writelane_b32 v248, s1, 22
	v_cmp_gt_i32_e64 s[0:1], 59, v208
	s_nop 1
	v_writelane_b32 v248, s0, 23
	s_nop 1
	v_writelane_b32 v248, s1, 24
	v_cmp_gt_i32_e64 s[0:1], 58, v208
	s_nop 1
	v_writelane_b32 v248, s0, 25
	s_nop 1
	v_writelane_b32 v248, s1, 26
	v_mov_b64_e32 v[50:51], 0
	v_mov_b64_e32 v[52:53], 0
	v_mov_b64_e32 v[54:55], 0
	v_mov_b64_e32 v[56:57], 0
	v_mov_b64_e32 v[58:59], 0
	v_mov_b64_e32 v[60:61], 0
	v_mov_b64_e32 v[62:63], 0
	v_mov_b64_e32 v[64:65], 0
	v_mov_b64_e32 v[66:67], 0
	v_mov_b64_e32 v[68:69], 0
	v_mov_b64_e32 v[70:71], 0
	v_mov_b64_e32 v[72:73], 0
	v_mov_b64_e32 v[74:75], 0
	v_mov_b64_e32 v[76:77], 0
	v_mov_b64_e32 v[78:79], 0
	v_mov_b64_e32 v[80:81], 0
	s_mov_b32 s32, 0x8000
	s_add_i32 s99, s82, -5
	s_max_i32 s99, s99, 0
	s_cmp_gt_i32 s80, 5
	s_cbranch_scc1 .Lnsa_e6_win
	s_sub_i32 s0, 5, s80
	s_lshl_b32 s0, s0, 13
	v_readlane_b32 s100, v251, 59
	v_readlane_b32 s101, v251, 61
	s_branch .Lnsa_e6_done

.LBB0_599:
	s_cmp_eq_u32 s2, s81
	s_cselect_b64 s[84:85], -1, 0
	s_cbranch_scc0 .LBB0_601
	v_mov_b32_e32 v3, v114
	s_nop 1
	v_permlane32_swap_b32_e32 v114, v3
	v_add_f32_e32 v3, v114, v3
	v_div_scale_f32 v4, s[0:1], v3, v3, 1.0
	v_rcp_f32_e32 v5, v4
	s_waitcnt lgkmcnt(0)
	ds_read_b32 v211, v210
	v_mov_b32_e32 v16, v2
	v_mov_b32_e32 v17, v2
	v_fma_f32 v6, -v4, v5, 1.0
	v_fmac_f32_e32 v5, v6, v5
	v_div_scale_f32 v6, vcc, 1.0, v3, 1.0
	v_mul_f32_e32 v7, v6, v5
	v_fma_f32 v8, -v4, v7, v6
	v_fmac_f32_e32 v7, v8, v5
	v_fma_f32 v4, -v4, v7, v6
	v_div_fmas_f32 v4, v4, v5, v7
	v_div_fixup_f32 v4, v4, v3, 1.0
	v_cmp_lt_f32_e32 vcc, 0, v3
	v_mov_b32_e32 v6, v2
	v_mov_b32_e32 v7, v2
	v_cndmask_b32_e32 v3, 0, v4, vcc
	v_mul_f32_e32 v4, v200, v3
	v_pk_fma_f32 v[48:49], v[80:81], v[4:5], v[48:49] op_sel_hi:[1,0,1]
	v_pk_fma_f32 v[46:47], v[78:79], v[4:5], v[46:47] op_sel_hi:[1,0,1]
	v_pk_fma_f32 v[44:45], v[76:77], v[4:5], v[44:45] op_sel_hi:[1,0,1]
	v_pk_fma_f32 v[42:43], v[74:75], v[4:5], v[42:43] op_sel_hi:[1,0,1]
	v_pk_fma_f32 v[40:41], v[72:73], v[4:5], v[40:41] op_sel_hi:[1,0,1]
	v_pk_fma_f32 v[38:39], v[70:71], v[4:5], v[38:39] op_sel_hi:[1,0,1]
	v_pk_fma_f32 v[36:37], v[68:69], v[4:5], v[36:37] op_sel_hi:[1,0,1]
	v_pk_fma_f32 v[34:35], v[66:67], v[4:5], v[34:35] op_sel_hi:[1,0,1]
	v_pk_fma_f32 v[32:33], v[64:65], v[4:5], v[32:33] op_sel_hi:[1,0,1]
	v_pk_fma_f32 v[30:31], v[62:63], v[4:5], v[30:31] op_sel_hi:[1,0,1]
	v_pk_fma_f32 v[28:29], v[60:61], v[4:5], v[28:29] op_sel_hi:[1,0,1]
	v_pk_fma_f32 v[26:27], v[58:59], v[4:5], v[26:27] op_sel_hi:[1,0,1]
	v_pk_fma_f32 v[24:25], v[56:57], v[4:5], v[24:25] op_sel_hi:[1,0,1]
	v_pk_fma_f32 v[22:23], v[54:55], v[4:5], v[22:23] op_sel_hi:[1,0,1]
	v_pk_fma_f32 v[20:21], v[52:53], v[4:5], v[20:21] op_sel_hi:[1,0,1]
	v_pk_fma_f32 v[18:19], v[50:51], v[4:5], v[18:19] op_sel_hi:[1,0,1]
	v_mov_b32_e32 v3, v2
	v_mov_b32_e32 v4, v2
	v_mov_b32_e32 v5, v2
	v_mov_b32_e32 v8, v2
	v_mov_b32_e32 v9, v2
	v_mov_b32_e32 v10, v2
	v_mov_b32_e32 v11, v2
	v_mov_b32_e32 v12, v2
	v_mov_b32_e32 v13, v2
	v_mov_b32_e32 v14, v2
	v_mov_b32_e32 v15, v2
	v_mov_b64_e32 v[64:65], v[16:17]
	v_mov_b64_e32 v[80:81], v[16:17]
	v_mov_b32_e32 v213, 0
	v_mov_b64_e32 v[62:63], v[14:15]
	v_mov_b64_e32 v[60:61], v[12:13]
	v_mov_b64_e32 v[58:59], v[10:11]
	v_mov_b64_e32 v[56:57], v[8:9]
	v_mov_b64_e32 v[54:55], v[6:7]
	v_mov_b64_e32 v[52:53], v[4:5]
	v_mov_b64_e32 v[50:51], v[2:3]
	v_mov_b64_e32 v[78:79], v[14:15]
	v_mov_b64_e32 v[76:77], v[12:13]
	v_mov_b64_e32 v[74:75], v[10:11]
	v_mov_b64_e32 v[72:73], v[8:9]
	v_mov_b64_e32 v[70:71], v[6:7]
	v_mov_b64_e32 v[68:69], v[4:5]
	v_mov_b64_e32 v[66:67], v[2:3]
	v_mov_b32_e32 v3, 0
	s_branch .LBB0_602

.LBB0_602:
	s_mov_b32 s3, s32
	s_cmp_gt_u32 s2, s80
	s_cbranch_scc1 .Lnsa_sel_entry
	s_add_i32 s76, s2, s79
	s_cmp_eq_u32 s78, s76
	s_mov_b64 s[0:1], -1
	s_cbranch_scc1 .LBB0_607
	s_and_b64 vcc, s[94:95], s[86:87]
	s_cbranch_vccnz .LBB0_607
	v_add3_u32 v16, s3, v203, v202
	ds_read_b128 v[4:7], v16
	ds_read_b128 v[8:11], v16 offset:512
	ds_read_b128 v[12:15], v16 offset:2048
	ds_read_b128 v[82:85], v16 offset:2560
	ds_read_b128 v[86:89], v16 offset:4096
	ds_read_b128 v[90:93], v16 offset:4608
	ds_read_b128 v[94:97], v16 offset:6144
	ds_read_b128 v[98:101], v16 offset:6656
	v_xor_b32_e32 v114, 0x80000000, v3
	v_mov_b32_e32 v115, v114
	v_mov_b32_e32 v116, v114
	v_mov_b32_e32 v117, v114
	v_mov_b32_e32 v118, v114
	v_mov_b32_e32 v119, v114
	v_mov_b32_e32 v120, v114
	v_mov_b32_e32 v121, v114
	v_mov_b32_e32 v122, v114
	v_mov_b32_e32 v123, v114
	v_mov_b32_e32 v124, v114
	v_mov_b32_e32 v125, v114
	v_mov_b32_e32 v126, v114
	v_mov_b32_e32 v127, v114
	v_mov_b32_e32 v128, v114
	v_mov_b32_e32 v129, v114
	s_waitcnt lgkmcnt(7)
	s_nop 0
	v_mfma_f32_32x32x16_bf16 v[130:145], v[4:7], v[158:161], v[114:129]
	v_add_u32_e32 v6, s3, v229
	s_waitcnt lgkmcnt(6)
	v_mfma_f32_32x32x16_bf16 v[114:129], v[8:11], v[158:161], v[114:129]
	s_waitcnt lgkmcnt(5)
	v_mfma_f32_32x32x16_bf16 v[130:145], v[12:15], v[154:157], v[130:145]
	ds_read_b64_tr_b16 v[178:179], v6 offset:8192
	ds_read_b64_tr_b16 v[180:181], v6 offset:8704
	ds_read_b64_tr_b16 v[174:175], v6 offset:12288
	ds_read_b64_tr_b16 v[176:177], v6 offset:12800
	ds_read_b64_tr_b16 v[170:171], v6 offset:9216
	ds_read_b64_tr_b16 v[172:173], v6 offset:9728
	ds_read_b64_tr_b16 v[166:167], v6 offset:13312
	ds_read_b64_tr_b16 v[168:169], v6 offset:13824
	ds_read_b64_tr_b16 v[162:163], v6 offset:10240
	ds_read_b64_tr_b16 v[164:165], v6 offset:10752
	ds_read_b64_tr_b16 v[12:13], v6 offset:14336
	ds_read_b64_tr_b16 v[14:15], v6 offset:14848
	ds_read_b64_tr_b16 v[8:9], v6 offset:11264
	ds_read_b64_tr_b16 v[10:11], v6 offset:11776
	ds_read_b64_tr_b16 v[4:5], v6 offset:15360
	ds_read_b64_tr_b16 v[6:7], v6 offset:15872
	s_waitcnt lgkmcnt(14)
	v_mfma_f32_32x32x16_bf16 v[114:129], v[82:85], v[154:157], v[114:129]
	v_mfma_f32_32x32x16_bf16 v[130:145], v[86:89], v[150:153], v[130:145]
	v_mfma_f32_32x32x16_bf16 v[114:129], v[90:93], v[150:153], v[114:129]
	v_mfma_f32_32x32x16_bf16 v[130:145], v[94:97], v[146:149], v[130:145]
	v_mfma_f32_32x32x16_bf16 v[114:129], v[98:101], v[146:149], v[114:129]
	s_nop 10
	v_max_f32_e32 v16, v130, v131
	v_max3_f32 v17, v132, v133, v115
	v_max3_f32 v16, v16, v114, v116
	v_max3_f32 v16, v16, v117, v134
	v_max3_f32 v17, v17, v136, v137
	v_max3_f32 v16, v16, v135, v118
	v_max3_f32 v17, v17, v120, v121
	v_max3_f32 v16, v16, v119, v138
	v_max3_f32 v17, v17, v140, v141
	v_max3_f32 v16, v16, v139, v122
	v_max3_f32 v17, v17, v124, v125
	v_max3_f32 v16, v16, v123, v142
	v_max3_f32 v17, v17, v144, v145
	v_max3_f32 v16, v16, v143, v126
	v_max3_f32 v17, v17, v128, v129
	v_max3_f32 v16, v16, v127, v17
	v_mov_b32_e32 v17, v16
	s_nop 1
	v_permlane32_swap_b32_e32 v16, v17
	v_max_f32_e32 v17, v16, v17
	s_mov_b32 s0, 0x41000000
	v_cmp_lt_f32_e32 vcc, s0, v17
	s_or_b64 vcc, vcc, s[86:87]
	v_mov_b32_e32 v16, v213
	v_mov_b32_e32 v214, v3
	s_cbranch_vccz .LBB0_606
	v_cndmask_b32_e64 v16, 0, v197, s[86:87]
	v_max_f32_e32 v17, v17, v17
	v_max_f32_e32 v16, v17, v16
	v_exp_f32_e64 v216, -v16
	v_add_f32_e32 v214, v3, v16
	v_pk_add_f32 v[130:131], v[130:131], v[16:17] op_sel_hi:[1,0] neg_lo:[0,1] neg_hi:[0,1]
	v_pk_add_f32 v[114:115], v[114:115], v[16:17] op_sel_hi:[1,0] neg_lo:[0,1] neg_hi:[0,1]
	v_pk_add_f32 v[132:133], v[132:133], v[16:17] op_sel_hi:[1,0] neg_lo:[0,1] neg_hi:[0,1]
	v_pk_add_f32 v[116:117], v[116:117], v[16:17] op_sel_hi:[1,0] neg_lo:[0,1] neg_hi:[0,1]
	v_pk_add_f32 v[134:135], v[134:135], v[16:17] op_sel_hi:[1,0] neg_lo:[0,1] neg_hi:[0,1]
	v_pk_add_f32 v[118:119], v[118:119], v[16:17] op_sel_hi:[1,0] neg_lo:[0,1] neg_hi:[0,1]
	v_pk_add_f32 v[136:137], v[136:137], v[16:17] op_sel_hi:[1,0] neg_lo:[0,1] neg_hi:[0,1]
	v_pk_add_f32 v[120:121], v[120:121], v[16:17] op_sel_hi:[1,0] neg_lo:[0,1] neg_hi:[0,1]
	v_pk_add_f32 v[138:139], v[138:139], v[16:17] op_sel_hi:[1,0] neg_lo:[0,1] neg_hi:[0,1]
	v_pk_add_f32 v[122:123], v[122:123], v[16:17] op_sel_hi:[1,0] neg_lo:[0,1] neg_hi:[0,1]
	v_pk_add_f32 v[140:141], v[140:141], v[16:17] op_sel_hi:[1,0] neg_lo:[0,1] neg_hi:[0,1]
	v_pk_add_f32 v[124:125], v[124:125], v[16:17] op_sel_hi:[1,0] neg_lo:[0,1] neg_hi:[0,1]
	v_pk_add_f32 v[142:143], v[142:143], v[16:17] op_sel_hi:[1,0] neg_lo:[0,1] neg_hi:[0,1]
	v_pk_add_f32 v[126:127], v[126:127], v[16:17] op_sel_hi:[1,0] neg_lo:[0,1] neg_hi:[0,1]
	v_pk_add_f32 v[144:145], v[144:145], v[16:17] op_sel_hi:[1,0] neg_lo:[0,1] neg_hi:[0,1]
	v_pk_add_f32 v[128:129], v[128:129], v[16:17] op_sel_hi:[1,0] neg_lo:[0,1] neg_hi:[0,1]
	v_pk_mul_f32 v[80:81], v[80:81], v[216:217] op_sel_hi:[1,0]
	v_pk_mul_f32 v[78:79], v[78:79], v[216:217] op_sel_hi:[1,0]
	v_pk_mul_f32 v[76:77], v[76:77], v[216:217] op_sel_hi:[1,0]
	v_pk_mul_f32 v[74:75], v[74:75], v[216:217] op_sel_hi:[1,0]
	v_pk_mul_f32 v[72:73], v[72:73], v[216:217] op_sel_hi:[1,0]
	v_pk_mul_f32 v[70:71], v[70:71], v[216:217] op_sel_hi:[1,0]
	v_pk_mul_f32 v[68:69], v[68:69], v[216:217] op_sel_hi:[1,0]
	v_pk_mul_f32 v[66:67], v[66:67], v[216:217] op_sel_hi:[1,0]
	v_pk_mul_f32 v[64:65], v[64:65], v[216:217] op_sel_hi:[1,0]
	v_pk_mul_f32 v[62:63], v[62:63], v[216:217] op_sel_hi:[1,0]
	v_pk_mul_f32 v[60:61], v[60:61], v[216:217] op_sel_hi:[1,0]
	v_pk_mul_f32 v[58:59], v[58:59], v[216:217] op_sel_hi:[1,0]
	v_pk_mul_f32 v[56:57], v[56:57], v[216:217] op_sel_hi:[1,0]
	v_pk_mul_f32 v[54:55], v[54:55], v[216:217] op_sel_hi:[1,0]
	v_pk_mul_f32 v[52:53], v[52:53], v[216:217] op_sel_hi:[1,0]
	v_pk_mul_f32 v[50:51], v[50:51], v[216:217] op_sel_hi:[1,0]
	v_mul_f32_e32 v16, v213, v216
.LBB0_606:
	v_exp_f32_e32 v216, v130
	v_exp_f32_e32 v218, v131
	v_exp_f32_e32 v220, v132
	v_exp_f32_e32 v222, v133
	v_exp_f32_e32 v134, v134
	v_exp_f32_e32 v224, v135
	v_exp_f32_e32 v136, v136
	v_exp_f32_e32 v226, v137
	v_exp_f32_e32 v217, v114
	v_cvt_pk_bf16_f32 v130, v216, v218
	v_cvt_pk_bf16_f32 v131, v220, v222
	v_cvt_pk_bf16_f32 v132, v134, v224
	v_cvt_pk_bf16_f32 v133, v136, v226
	v_exp_f32_e32 v219, v115
	v_pk_add_f32 v[114:115], v[216:217], 0 op_sel_hi:[1,0]
	v_mfma_f32_32x32x16_bf16 v[66:81], v[178:181], v[130:133], v[66:81]
	v_exp_f32_e32 v221, v116
	v_exp_f32_e32 v138, v138
	v_exp_f32_e32 v180, v139
	v_exp_f32_e32 v140, v140
	v_exp_f32_e32 v216, v141
	v_exp_f32_e32 v142, v142
	v_pk_add_f32 v[114:115], v[218:219], v[114:115]
	s_waitcnt lgkmcnt(12)
	v_mfma_f32_32x32x16_bf16 v[50:65], v[174:177], v[130:133], v[50:65]
	v_exp_f32_e32 v130, v143
	v_exp_f32_e32 v132, v144
	v_exp_f32_e32 v144, v145
	v_pk_add_f32 v[178:179], v[220:221], v[114:115]
	v_exp_f32_e32 v223, v117
	v_cvt_pk_bf16_f32 v114, v138, v180
	v_cvt_pk_bf16_f32 v115, v140, v216
	v_cvt_pk_bf16_f32 v116, v142, v130
	v_cvt_pk_bf16_f32 v117, v132, v144
	v_exp_f32_e32 v135, v118
	v_exp_f32_e32 v225, v119
	s_waitcnt lgkmcnt(10)
	v_mfma_f32_32x32x16_bf16 v[66:81], v[170:173], v[114:117], v[66:81]
	v_exp_f32_e32 v137, v120
	v_exp_f32_e32 v227, v121
	v_pk_add_f32 v[118:119], v[222:223], v[178:179]
	v_exp_f32_e32 v139, v122
	v_pk_add_f32 v[118:119], v[134:135], v[118:119]
	v_exp_f32_e32 v181, v123
	v_pk_add_f32 v[118:119], v[224:225], v[118:119]
	s_waitcnt lgkmcnt(8)
	v_mfma_f32_32x32x16_bf16 v[50:65], v[166:169], v[114:117], v[50:65]
	v_cvt_pk_bf16_f32 v114, v217, v219
	v_cvt_pk_bf16_f32 v115, v221, v223
	v_cvt_pk_bf16_f32 v116, v135, v225
	v_cvt_pk_bf16_f32 v117, v137, v227
	v_exp_f32_e32 v141, v124
	v_exp_f32_e32 v217, v125
	v_exp_f32_e32 v143, v126
	s_waitcnt lgkmcnt(6)
	v_mfma_f32_32x32x16_bf16 v[66:81], v[162:165], v[114:117], v[66:81]
	v_exp_f32_e32 v131, v127
	v_exp_f32_e32 v133, v128
	v_exp_f32_e32 v145, v129
	v_pk_add_f32 v[118:119], v[136:137], v[118:119]
	v_pk_add_f32 v[118:119], v[226:227], v[118:119]
	s_waitcnt lgkmcnt(4)
	v_mfma_f32_32x32x16_bf16 v[50:65], v[12:15], v[114:117], v[50:65]
	v_add_f32_e64 v118, v138, v118
	v_add_f32_e64 v119, v139, v119
	v_cvt_pk_bf16_f32 v12, v139, v181
	v_add_f32_e64 v118, v180, v118
	v_add_f32_e64 v119, v181, v119
	v_cvt_pk_bf16_f32 v13, v141, v217
	v_cvt_pk_bf16_f32 v14, v143, v131
	v_cvt_pk_bf16_f32 v15, v133, v145
	v_pk_add_f32 v[118:119], v[140:141], v[118:119]
	s_waitcnt lgkmcnt(2)
	v_mfma_f32_32x32x16_bf16 v[66:81], v[8:11], v[12:15], v[66:81]
	v_add_f32_e64 v8, v216, v118
	v_add_f32_e64 v9, v217, v119
	v_add_f32_e64 v8, v142, v8
	v_add_f32_e64 v9, v143, v9
	v_add_f32_e64 v8, v130, v8
	v_add_f32_e64 v9, v131, v9
	v_pk_add_f32 v[8:9], v[132:133], v[8:9]
	s_waitcnt lgkmcnt(0)
	v_mfma_f32_32x32x16_bf16 v[50:65], v[4:7], v[12:15], v[50:65]
	v_add_f32_e64 v8, v144, v8
	v_add_f32_e64 v9, v145, v9
	v_add_f32_e32 v8, v8, v9
	v_add_f32_e32 v114, v16, v8
	s_branch .LBB0_626
.LBB0_607:
	s_and_b64 vcc, exec, s[0:1]
	s_cbranch_vccz .LBB0_616
	v_add3_u32 v16, s3, v203, v202
	ds_read_b128 v[4:7], v16
	ds_read_b128 v[8:11], v16 offset:512
	ds_read_b128 v[12:15], v16 offset:2048
	ds_read_b128 v[114:117], v16 offset:2560
	ds_read_b128 v[118:121], v16 offset:4096
	ds_read_b128 v[122:125], v16 offset:4608
	ds_read_b128 v[126:129], v16 offset:6144
	ds_read_b128 v[130:133], v16 offset:6656
	v_xor_b32_e32 v82, 0x80000000, v3
	s_sub_i32 s0, s78, s76
	v_mov_b32_e32 v83, v82
	v_mov_b32_e32 v84, v82
	v_mov_b32_e32 v85, v82
	v_mov_b32_e32 v86, v82
	v_mov_b32_e32 v87, v82
	v_mov_b32_e32 v88, v82
	v_mov_b32_e32 v89, v82
	v_mov_b32_e32 v90, v82
	v_mov_b32_e32 v91, v82
	v_mov_b32_e32 v92, v82
	v_mov_b32_e32 v93, v82
	v_mov_b32_e32 v94, v82
	v_mov_b32_e32 v95, v82
	v_mov_b32_e32 v96, v82
	v_mov_b32_e32 v97, v82
	s_waitcnt lgkmcnt(7)
	s_nop 0
	v_mfma_f32_32x32x16_bf16 v[98:113], v[4:7], v[158:161], v[82:97]
	v_add_u32_e32 v6, s3, v229
	s_waitcnt lgkmcnt(6)
	v_mfma_f32_32x32x16_bf16 v[82:97], v[8:11], v[158:161], v[82:97]
	s_waitcnt lgkmcnt(5)
	v_mfma_f32_32x32x16_bf16 v[98:113], v[12:15], v[154:157], v[98:113]
	s_waitcnt lgkmcnt(4)
	v_mfma_f32_32x32x16_bf16 v[82:97], v[114:117], v[154:157], v[82:97]
	s_waitcnt lgkmcnt(3)
	v_mfma_f32_32x32x16_bf16 v[98:113], v[118:121], v[150:153], v[98:113]
	s_waitcnt lgkmcnt(2)
	v_mfma_f32_32x32x16_bf16 v[82:97], v[122:125], v[150:153], v[82:97]
	s_waitcnt lgkmcnt(1)
	v_mfma_f32_32x32x16_bf16 v[98:113], v[126:129], v[146:149], v[98:113]
	s_waitcnt lgkmcnt(0)
	v_mfma_f32_32x32x16_bf16 v[82:97], v[130:133], v[146:149], v[82:97]
	ds_read_b64_tr_b16 v[130:131], v6 offset:8192
	ds_read_b64_tr_b16 v[132:133], v6 offset:8704
	ds_read_b64_tr_b16 v[126:127], v6 offset:12288
	ds_read_b64_tr_b16 v[128:129], v6 offset:12800
	ds_read_b64_tr_b16 v[122:123], v6 offset:9216
	ds_read_b64_tr_b16 v[124:125], v6 offset:9728
	ds_read_b64_tr_b16 v[118:119], v6 offset:13312
	ds_read_b64_tr_b16 v[120:121], v6 offset:13824
	ds_read_b64_tr_b16 v[114:115], v6 offset:10240
	ds_read_b64_tr_b16 v[116:117], v6 offset:10752
	ds_read_b64_tr_b16 v[12:13], v6 offset:14336
	ds_read_b64_tr_b16 v[14:15], v6 offset:14848
	ds_read_b64_tr_b16 v[8:9], v6 offset:11264
	ds_read_b64_tr_b16 v[10:11], v6 offset:11776
	ds_read_b64_tr_b16 v[4:5], v6 offset:15360
	ds_read_b64_tr_b16 v[6:7], v6 offset:15872
	v_lshl_add_u32 v143, s0, 6, v208
	v_add_u32_e32 v16, -1, v143
	v_cmp_gt_u32_e32 vcc, s77, v16
	v_subrev_u32_e32 v16, 33, v143
	v_subrev_u32_e32 v17, 32, v143
	v_cndmask_b32_e32 v169, v195, v99, vcc
	v_cmp_gt_u32_e32 vcc, s77, v143
	s_mov_b32 s0, 0x41000000
	s_nop 0
	v_cndmask_b32_e32 v172, v195, v98, vcc
	v_cmp_gt_u32_e32 vcc, s77, v16
	v_add_u32_e32 v16, -3, v143
	s_nop 0
	v_cndmask_b32_e32 v171, v195, v83, vcc
	v_cmp_gt_u32_e32 vcc, s77, v17
	v_add_u32_e32 v17, -2, v143
	v_add_u32_e32 v83, -10, v143
	v_cndmask_b32_e32 v176, v195, v82, vcc
	v_cmp_gt_u32_e32 vcc, s77, v16
	v_subrev_u32_e32 v16, 35, v143
	v_add_u32_e32 v82, -11, v143
	v_cndmask_b32_e32 v170, v195, v101, vcc
	v_cmp_gt_u32_e32 vcc, s77, v17
	v_subrev_u32_e32 v17, 34, v143
	s_nop 0
	v_cndmask_b32_e32 v174, v195, v100, vcc
	v_cmp_gt_u32_e32 vcc, s77, v16
	v_add_u32_e32 v16, -9, v143
	s_nop 0
	v_cndmask_b32_e32 v135, v195, v85, vcc
	v_cmp_gt_u32_e32 vcc, s77, v17
	v_add_u32_e32 v17, -8, v143
	s_nop 0
	v_cndmask_b32_e32 v178, v195, v84, vcc
	v_cmp_gt_u32_e32 vcc, s77, v16
	v_subrev_u32_e32 v16, 41, v143
	s_nop 0
	v_cndmask_b32_e32 v173, v195, v103, vcc
	v_cmp_gt_u32_e32 vcc, s77, v17
	v_subrev_u32_e32 v17, 40, v143
	s_nop 0
	v_cndmask_b32_e32 v177, v195, v102, vcc
	v_cmp_gt_u32_e32 vcc, s77, v16
	s_nop 1
	v_cndmask_b32_e32 v16, v195, v87, vcc
	v_cmp_gt_u32_e32 vcc, s77, v17
	s_nop 1
	v_cndmask_b32_e32 v17, v195, v86, vcc
	v_cmp_gt_u32_e32 vcc, s77, v82
	v_subrev_u32_e32 v82, 43, v143
	s_nop 0
	v_cndmask_b32_e32 v175, v195, v105, vcc
	v_cmp_gt_u32_e32 vcc, s77, v83
	v_subrev_u32_e32 v83, 42, v143
	s_nop 0
	v_cndmask_b32_e32 v179, v195, v104, vcc
	v_cmp_gt_u32_e32 vcc, s77, v82
	v_subrev_u32_e32 v82, 17, v143
	s_nop 0
	v_cndmask_b32_e32 v134, v195, v89, vcc
	v_cmp_gt_u32_e32 vcc, s77, v83
	v_add_u32_e32 v83, -16, v143
	s_nop 0
	v_cndmask_b32_e32 v137, v195, v88, vcc
	v_cmp_gt_u32_e32 vcc, s77, v82
	v_subrev_u32_e32 v82, 49, v143
	s_nop 0
	v_cndmask_b32_e32 v145, v195, v107, vcc
	v_cmp_gt_u32_e32 vcc, s77, v83
	v_subrev_u32_e32 v83, 48, v143
	s_nop 0
	v_cndmask_b32_e32 v162, v195, v106, vcc
	v_cmp_gt_u32_e32 vcc, s77, v82
	v_subrev_u32_e32 v82, 19, v143
	s_nop 0
	v_cndmask_b32_e32 v138, v195, v91, vcc
	v_cmp_gt_u32_e32 vcc, s77, v83
	v_subrev_u32_e32 v83, 18, v143
	s_nop 0
	v_cndmask_b32_e32 v140, v195, v90, vcc
	v_cmp_gt_u32_e32 vcc, s77, v82
	v_subrev_u32_e32 v82, 51, v143
	s_nop 0
	v_cndmask_b32_e32 v163, v195, v109, vcc
	v_cmp_gt_u32_e32 vcc, s77, v83
	v_subrev_u32_e32 v83, 50, v143
	s_nop 0
	v_cndmask_b32_e32 v164, v195, v108, vcc
	v_cmp_gt_u32_e32 vcc, s77, v82
	v_subrev_u32_e32 v82, 25, v143
	s_nop 0
	v_cndmask_b32_e32 v136, v195, v93, vcc
	v_cmp_gt_u32_e32 vcc, s77, v83
	v_subrev_u32_e32 v83, 24, v143
	s_nop 0
	v_cndmask_b32_e32 v139, v195, v92, vcc
	v_cmp_gt_u32_e32 vcc, s77, v82
	v_subrev_u32_e32 v82, 57, v143
	s_nop 0
	v_cndmask_b32_e32 v165, v195, v111, vcc
	v_cmp_gt_u32_e32 vcc, s77, v83
	v_subrev_u32_e32 v83, 56, v143
	s_nop 0
	v_cndmask_b32_e32 v166, v195, v110, vcc
	v_cmp_gt_u32_e32 vcc, s77, v82
	v_subrev_u32_e32 v82, 27, v143
	s_nop 0
	v_cndmask_b32_e32 v141, v195, v95, vcc
	v_cmp_gt_u32_e32 vcc, s77, v83
	v_subrev_u32_e32 v83, 26, v143
	s_nop 0
	v_cndmask_b32_e32 v142, v195, v94, vcc
	v_cmp_gt_u32_e32 vcc, s77, v82
	v_subrev_u32_e32 v82, 59, v143
	s_nop 0
	v_cndmask_b32_e32 v167, v195, v113, vcc
	v_cmp_gt_u32_e32 vcc, s77, v83
	v_subrev_u32_e32 v83, 58, v143
	s_nop 0
	v_cndmask_b32_e32 v168, v195, v112, vcc
	v_cmp_gt_u32_e32 vcc, s77, v82
	v_max_f32_e32 v82, v169, v169
	s_nop 0
	v_cndmask_b32_e32 v143, v195, v97, vcc
	v_cmp_gt_u32_e32 vcc, s77, v83
	v_max_f32_e32 v83, v172, v172
	v_max_f32_e32 v82, v83, v82
	v_max3_f32 v83, v174, v170, v171
	v_max3_f32 v82, v82, v176, v178
	v_max3_f32 v82, v82, v135, v177
	v_max3_f32 v83, v83, v179, v175
	v_max3_f32 v82, v82, v173, v17
	v_max3_f32 v83, v83, v137, v134
	v_max3_f32 v82, v82, v16, v162
	v_max3_f32 v83, v83, v164, v163
	v_max3_f32 v82, v82, v145, v140
	v_max3_f32 v83, v83, v139, v136
	v_cndmask_b32_e32 v144, v195, v96, vcc
	v_max3_f32 v82, v82, v138, v166
	v_max3_f32 v83, v83, v168, v167
	v_max3_f32 v82, v82, v165, v142
	v_max3_f32 v83, v83, v144, v143
	v_max3_f32 v82, v82, v141, v83
	v_mov_b32_e32 v83, v82
	s_nop 1
	v_permlane32_swap_b32_e32 v82, v83
	v_max_f32_e32 v83, v83, v83
	v_max_f32_e32 v82, v82, v82
	v_max_f32_e32 v82, v82, v83
	v_cmp_lt_f32_e32 vcc, s0, v82
	s_cmp_eq_u64 vcc, 0
	s_cselect_b64 s[0:1], -1, 0
	s_xor_b64 vcc, s[86:87], -1
	s_and_b64 s[0:1], vcc, s[0:1]
	s_and_b64 vcc, exec, s[0:1]
	s_cbranch_vccnz .LBB0_614
	v_cndmask_b32_e64 v83, 0, v197, s[86:87]
	v_max_f32_e32 v82, v82, v82
	v_max_f32_e32 v82, v82, v83
	v_exp_f32_e64 v180, -v82
	v_add_f32_e32 v214, v3, v82
	v_sub_f32_e32 v172, v172, v82
	v_sub_f32_e32 v169, v169, v82
	v_sub_f32_e32 v174, v174, v82
	v_sub_f32_e32 v170, v170, v82
	v_sub_f32_e32 v177, v177, v82
	v_sub_f32_e32 v173, v173, v82
	v_sub_f32_e32 v179, v179, v82
	v_sub_f32_e32 v175, v175, v82
	v_sub_f32_e32 v162, v162, v82
	v_sub_f32_e32 v145, v145, v82
	v_sub_f32_e32 v164, v164, v82
	v_sub_f32_e32 v163, v163, v82
	v_sub_f32_e32 v166, v166, v82
	v_sub_f32_e32 v165, v165, v82
	v_sub_f32_e32 v168, v168, v82
	v_sub_f32_e32 v167, v167, v82
	v_sub_f32_e32 v176, v176, v82
	v_sub_f32_e32 v171, v171, v82
	v_sub_f32_e32 v178, v178, v82
	v_sub_f32_e32 v135, v135, v82
	v_sub_f32_e32 v17, v17, v82
	v_sub_f32_e32 v16, v16, v82
	v_sub_f32_e32 v137, v137, v82
	v_sub_f32_e32 v134, v134, v82
	v_sub_f32_e32 v140, v140, v82
	v_sub_f32_e32 v138, v138, v82
	v_sub_f32_e32 v139, v139, v82
	v_sub_f32_e32 v136, v136, v82
	v_sub_f32_e32 v142, v142, v82
	v_sub_f32_e32 v141, v141, v82
	v_sub_f32_e32 v144, v144, v82
	v_sub_f32_e32 v143, v143, v82
	v_pk_mul_f32 v[80:81], v[80:81], v[180:181] op_sel_hi:[1,0]
	v_pk_mul_f32 v[78:79], v[78:79], v[180:181] op_sel_hi:[1,0]
	v_pk_mul_f32 v[76:77], v[76:77], v[180:181] op_sel_hi:[1,0]
	v_pk_mul_f32 v[74:75], v[74:75], v[180:181] op_sel_hi:[1,0]
	v_pk_mul_f32 v[72:73], v[72:73], v[180:181] op_sel_hi:[1,0]
	v_pk_mul_f32 v[70:71], v[70:71], v[180:181] op_sel_hi:[1,0]
	v_pk_mul_f32 v[68:69], v[68:69], v[180:181] op_sel_hi:[1,0]
	v_pk_mul_f32 v[66:67], v[66:67], v[180:181] op_sel_hi:[1,0]
	v_pk_mul_f32 v[64:65], v[64:65], v[180:181] op_sel_hi:[1,0]
	v_pk_mul_f32 v[62:63], v[62:63], v[180:181] op_sel_hi:[1,0]
	v_pk_mul_f32 v[60:61], v[60:61], v[180:181] op_sel_hi:[1,0]
	v_pk_mul_f32 v[58:59], v[58:59], v[180:181] op_sel_hi:[1,0]
	v_pk_mul_f32 v[56:57], v[56:57], v[180:181] op_sel_hi:[1,0]
	v_pk_mul_f32 v[54:55], v[54:55], v[180:181] op_sel_hi:[1,0]
	v_pk_mul_f32 v[52:53], v[52:53], v[180:181] op_sel_hi:[1,0]
	v_pk_mul_f32 v[50:51], v[50:51], v[180:181] op_sel_hi:[1,0]
	v_mul_f32_e32 v180, v213, v180
	s_branch .LBB0_615

.Lnsa_sel_entry:
	s_sub_i32 s76, s2, s81
	s_cmp_lg_u32 s76, s78
	s_mov_b64 s[0:1], -1
	s_cbranch_scc0 .LBB0_622
	s_waitcnt lgkmcnt(0)
	v_lshrrev_b32_e32 v4, s76, v211
	v_and_b32_e32 v4, 1, v4
	v_add3_u32 v16, s3, v203, v202
	v_cmp_eq_u32_e32 vcc, 1, v4
	ds_read_b128 v[4:7], v16
	ds_read_b128 v[8:11], v16 offset:512
	ds_read_b128 v[12:15], v16 offset:2048
	ds_read_b128 v[82:85], v16 offset:2560
	ds_read_b128 v[86:89], v16 offset:4096
	ds_read_b128 v[90:93], v16 offset:4608
	ds_read_b128 v[94:97], v16 offset:6144
	ds_read_b128 v[98:101], v16 offset:6656
	v_cndmask_b32_e64 v114, v195, -v3, vcc
	v_mov_b32_e32 v115, v114
	v_mov_b32_e32 v116, v114
	v_mov_b32_e32 v117, v114
	v_mov_b32_e32 v118, v114
	v_mov_b32_e32 v119, v114
	v_mov_b32_e32 v120, v114
	v_mov_b32_e32 v121, v114
	v_mov_b32_e32 v122, v114
	v_mov_b32_e32 v123, v114
	v_mov_b32_e32 v124, v114
	v_mov_b32_e32 v125, v114
	v_mov_b32_e32 v126, v114
	v_mov_b32_e32 v127, v114
	v_mov_b32_e32 v128, v114
	v_mov_b32_e32 v129, v114
	s_waitcnt lgkmcnt(7)
	s_nop 0
	v_mfma_f32_32x32x16_bf16 v[130:145], v[4:7], v[158:161], v[114:129]
	v_add_u32_e32 v6, s3, v229
	s_waitcnt lgkmcnt(6)
	v_mfma_f32_32x32x16_bf16 v[114:129], v[8:11], v[158:161], v[114:129]
	s_waitcnt lgkmcnt(5)
	v_mfma_f32_32x32x16_bf16 v[130:145], v[12:15], v[154:157], v[130:145]
	ds_read_b64_tr_b16 v[178:179], v6 offset:8192
	ds_read_b64_tr_b16 v[180:181], v6 offset:8704
	ds_read_b64_tr_b16 v[174:175], v6 offset:12288
	ds_read_b64_tr_b16 v[176:177], v6 offset:12800
	ds_read_b64_tr_b16 v[170:171], v6 offset:9216
	ds_read_b64_tr_b16 v[172:173], v6 offset:9728
	ds_read_b64_tr_b16 v[166:167], v6 offset:13312
	ds_read_b64_tr_b16 v[168:169], v6 offset:13824
	ds_read_b64_tr_b16 v[162:163], v6 offset:10240
	ds_read_b64_tr_b16 v[164:165], v6 offset:10752
	ds_read_b64_tr_b16 v[12:13], v6 offset:14336
	ds_read_b64_tr_b16 v[14:15], v6 offset:14848
	ds_read_b64_tr_b16 v[8:9], v6 offset:11264
	ds_read_b64_tr_b16 v[10:11], v6 offset:11776
	ds_read_b64_tr_b16 v[4:5], v6 offset:15360
	ds_read_b64_tr_b16 v[6:7], v6 offset:15872
	s_waitcnt lgkmcnt(14)
	v_mfma_f32_32x32x16_bf16 v[114:129], v[82:85], v[154:157], v[114:129]
	v_mfma_f32_32x32x16_bf16 v[130:145], v[86:89], v[150:153], v[130:145]
	v_mfma_f32_32x32x16_bf16 v[114:129], v[90:93], v[150:153], v[114:129]
	v_mfma_f32_32x32x16_bf16 v[130:145], v[94:97], v[146:149], v[130:145]
	v_mfma_f32_32x32x16_bf16 v[114:129], v[98:101], v[146:149], v[114:129]
	s_nop 10
	v_max_f32_e32 v16, v130, v131
	v_max3_f32 v17, v132, v133, v115
	v_max3_f32 v16, v16, v114, v116
	v_max3_f32 v16, v16, v117, v134
	v_max3_f32 v17, v17, v136, v137
	v_max3_f32 v16, v16, v135, v118
	v_max3_f32 v17, v17, v120, v121
	v_max3_f32 v16, v16, v119, v138
	v_max3_f32 v17, v17, v140, v141
	v_max3_f32 v16, v16, v139, v122
	v_max3_f32 v17, v17, v124, v125
	v_max3_f32 v16, v16, v123, v142
	v_max3_f32 v17, v17, v144, v145
	v_max3_f32 v16, v16, v143, v126
	v_max3_f32 v17, v17, v128, v129
	v_max3_f32 v16, v16, v127, v17
	v_mov_b32_e32 v17, v16
	s_nop 1
	v_permlane32_swap_b32_e32 v16, v17
	v_max_f32_e32 v17, v16, v17
	s_mov_b32 s0, 0x41000000
	v_cmp_lt_f32_e32 vcc, s0, v17
	s_or_b64 vcc, vcc, s[84:85]
	v_mov_b32_e32 v16, v213
	v_mov_b32_e32 v214, v3
	s_cbranch_vccz .LBB0_621
	v_cndmask_b32_e64 v16, 0, v197, s[84:85]
	v_max_f32_e32 v17, v17, v17
	v_max_f32_e32 v16, v17, v16
	v_exp_f32_e64 v216, -v16
	v_add_f32_e32 v214, v3, v16
	v_pk_add_f32 v[130:131], v[130:131], v[16:17] op_sel_hi:[1,0] neg_lo:[0,1] neg_hi:[0,1]
	v_pk_add_f32 v[114:115], v[114:115], v[16:17] op_sel_hi:[1,0] neg_lo:[0,1] neg_hi:[0,1]
	v_pk_add_f32 v[132:133], v[132:133], v[16:17] op_sel_hi:[1,0] neg_lo:[0,1] neg_hi:[0,1]
	v_pk_add_f32 v[116:117], v[116:117], v[16:17] op_sel_hi:[1,0] neg_lo:[0,1] neg_hi:[0,1]
	v_pk_add_f32 v[134:135], v[134:135], v[16:17] op_sel_hi:[1,0] neg_lo:[0,1] neg_hi:[0,1]
	v_pk_add_f32 v[118:119], v[118:119], v[16:17] op_sel_hi:[1,0] neg_lo:[0,1] neg_hi:[0,1]
	v_pk_add_f32 v[136:137], v[136:137], v[16:17] op_sel_hi:[1,0] neg_lo:[0,1] neg_hi:[0,1]
	v_pk_add_f32 v[120:121], v[120:121], v[16:17] op_sel_hi:[1,0] neg_lo:[0,1] neg_hi:[0,1]
	v_pk_add_f32 v[138:139], v[138:139], v[16:17] op_sel_hi:[1,0] neg_lo:[0,1] neg_hi:[0,1]
	v_pk_add_f32 v[122:123], v[122:123], v[16:17] op_sel_hi:[1,0] neg_lo:[0,1] neg_hi:[0,1]
	v_pk_add_f32 v[140:141], v[140:141], v[16:17] op_sel_hi:[1,0] neg_lo:[0,1] neg_hi:[0,1]
	v_pk_add_f32 v[124:125], v[124:125], v[16:17] op_sel_hi:[1,0] neg_lo:[0,1] neg_hi:[0,1]
	v_pk_add_f32 v[142:143], v[142:143], v[16:17] op_sel_hi:[1,0] neg_lo:[0,1] neg_hi:[0,1]
	v_pk_add_f32 v[126:127], v[126:127], v[16:17] op_sel_hi:[1,0] neg_lo:[0,1] neg_hi:[0,1]
	v_pk_add_f32 v[144:145], v[144:145], v[16:17] op_sel_hi:[1,0] neg_lo:[0,1] neg_hi:[0,1]
	v_pk_add_f32 v[128:129], v[128:129], v[16:17] op_sel_hi:[1,0] neg_lo:[0,1] neg_hi:[0,1]
	v_pk_mul_f32 v[80:81], v[80:81], v[216:217] op_sel_hi:[1,0]
	v_pk_mul_f32 v[78:79], v[78:79], v[216:217] op_sel_hi:[1,0]
	v_pk_mul_f32 v[76:77], v[76:77], v[216:217] op_sel_hi:[1,0]
	v_pk_mul_f32 v[74:75], v[74:75], v[216:217] op_sel_hi:[1,0]
	v_pk_mul_f32 v[72:73], v[72:73], v[216:217] op_sel_hi:[1,0]
	v_pk_mul_f32 v[70:71], v[70:71], v[216:217] op_sel_hi:[1,0]
	v_pk_mul_f32 v[68:69], v[68:69], v[216:217] op_sel_hi:[1,0]
	v_pk_mul_f32 v[66:67], v[66:67], v[216:217] op_sel_hi:[1,0]
	v_pk_mul_f32 v[64:65], v[64:65], v[216:217] op_sel_hi:[1,0]
	v_pk_mul_f32 v[62:63], v[62:63], v[216:217] op_sel_hi:[1,0]
	v_pk_mul_f32 v[60:61], v[60:61], v[216:217] op_sel_hi:[1,0]
	v_pk_mul_f32 v[58:59], v[58:59], v[216:217] op_sel_hi:[1,0]
	v_pk_mul_f32 v[56:57], v[56:57], v[216:217] op_sel_hi:[1,0]
	v_pk_mul_f32 v[54:55], v[54:55], v[216:217] op_sel_hi:[1,0]
	v_pk_mul_f32 v[52:53], v[52:53], v[216:217] op_sel_hi:[1,0]
	v_pk_mul_f32 v[50:51], v[50:51], v[216:217] op_sel_hi:[1,0]
	v_mul_f32_e32 v16, v213, v216

.LBB0_622:
	s_and_b64 vcc, exec, s[0:1]
	s_cbranch_vccz .LBB0_626
	v_add3_u32 v16, s3, v203, v202
	ds_read_b128 v[4:7], v16
	ds_read_b128 v[8:11], v16 offset:512
	ds_read_b128 v[12:15], v16 offset:2048
	ds_read_b128 v[114:117], v16 offset:2560
	ds_read_b128 v[118:121], v16 offset:4096
	ds_read_b128 v[122:125], v16 offset:4608
	ds_read_b128 v[126:129], v16 offset:6144
	ds_read_b128 v[130:133], v16 offset:6656
	v_xor_b32_e32 v82, 0x80000000, v3
	v_mov_b32_e32 v83, v82
	v_mov_b32_e32 v84, v82
	v_mov_b32_e32 v85, v82
	v_mov_b32_e32 v86, v82
	v_mov_b32_e32 v87, v82
	v_mov_b32_e32 v88, v82
	v_mov_b32_e32 v89, v82
	v_mov_b32_e32 v90, v82
	v_mov_b32_e32 v91, v82
	v_mov_b32_e32 v92, v82
	v_mov_b32_e32 v93, v82
	v_mov_b32_e32 v94, v82
	v_mov_b32_e32 v95, v82
	v_mov_b32_e32 v96, v82
	v_mov_b32_e32 v97, v82
	s_waitcnt lgkmcnt(7)
	s_nop 0
	v_mfma_f32_32x32x16_bf16 v[98:113], v[4:7], v[158:161], v[82:97]
	v_add_u32_e32 v6, s3, v229
	s_waitcnt lgkmcnt(6)
	v_mfma_f32_32x32x16_bf16 v[82:97], v[8:11], v[158:161], v[82:97]
	s_waitcnt lgkmcnt(5)
	v_mfma_f32_32x32x16_bf16 v[98:113], v[12:15], v[154:157], v[98:113]
	s_waitcnt lgkmcnt(4)
	v_mfma_f32_32x32x16_bf16 v[82:97], v[114:117], v[154:157], v[82:97]
	s_waitcnt lgkmcnt(3)
	v_mfma_f32_32x32x16_bf16 v[98:113], v[118:121], v[150:153], v[98:113]
	s_waitcnt lgkmcnt(2)
	v_mfma_f32_32x32x16_bf16 v[82:97], v[122:125], v[150:153], v[82:97]
	s_waitcnt lgkmcnt(1)
	v_mfma_f32_32x32x16_bf16 v[98:113], v[126:129], v[146:149], v[98:113]
	s_waitcnt lgkmcnt(0)
	v_mfma_f32_32x32x16_bf16 v[82:97], v[130:133], v[146:149], v[82:97]
	ds_read_b64_tr_b16 v[130:131], v6 offset:8192
	ds_read_b64_tr_b16 v[132:133], v6 offset:8704
	ds_read_b64_tr_b16 v[126:127], v6 offset:12288
	ds_read_b64_tr_b16 v[128:129], v6 offset:12800
	ds_read_b64_tr_b16 v[122:123], v6 offset:9216
	ds_read_b64_tr_b16 v[124:125], v6 offset:9728
	ds_read_b64_tr_b16 v[118:119], v6 offset:13312
	ds_read_b64_tr_b16 v[120:121], v6 offset:13824
	ds_read_b64_tr_b16 v[114:115], v6 offset:10240
	ds_read_b64_tr_b16 v[116:117], v6 offset:10752
	ds_read_b64_tr_b16 v[12:13], v6 offset:14336
	ds_read_b64_tr_b16 v[14:15], v6 offset:14848
	ds_read_b64_tr_b16 v[8:9], v6 offset:11264
	ds_read_b64_tr_b16 v[10:11], v6 offset:11776
	ds_read_b64_tr_b16 v[4:5], v6 offset:15360
	ds_read_b64_tr_b16 v[6:7], v6 offset:15872
	v_readlane_b32 s0, v249, 27
	v_readlane_b32 s1, v249, 28
	s_nop 1
	v_cndmask_b32_e64 v134, v99, v195, s[0:1]
	v_readlane_b32 s0, v249, 29
	v_readlane_b32 s1, v249, 30
	s_nop 1
	v_cndmask_b32_e64 v137, v98, v195, s[0:1]
	v_readlane_b32 s0, v249, 31
	v_readlane_b32 s1, v249, 32
	s_nop 1
	v_cndmask_b32_e64 v136, v83, v195, s[0:1]
	v_readlane_b32 s0, v249, 33
	v_readlane_b32 s1, v249, 34
	s_nop 1
	v_cndmask_b32_e64 v140, v82, v195, s[0:1]
	v_readlane_b32 s0, v249, 35
	v_readlane_b32 s1, v249, 36
	s_nop 1
	v_cndmask_b32_e64 v135, v101, v195, s[0:1]
	v_readlane_b32 s0, v249, 37
	v_readlane_b32 s1, v249, 38
	s_nop 1
	v_cndmask_b32_e64 v138, v100, v195, s[0:1]
	v_readlane_b32 s0, v249, 39
	v_readlane_b32 s1, v249, 40
	s_nop 1
	v_cndmask_b32_e64 v85, v85, v195, s[0:1]
	v_readlane_b32 s0, v249, 41
	v_readlane_b32 s1, v249, 42
	s_nop 1
	v_cndmask_b32_e64 v141, v84, v195, s[0:1]
	v_readlane_b32 s0, v249, 43
	v_readlane_b32 s1, v249, 44
	s_nop 1
	v_cndmask_b32_e64 v103, v103, v195, s[0:1]
	v_readlane_b32 s0, v249, 45
	v_readlane_b32 s1, v249, 46
	s_nop 1
	v_cndmask_b32_e64 v139, v102, v195, s[0:1]
	v_readlane_b32 s0, v249, 47
	v_readlane_b32 s1, v249, 48
	s_nop 1
	v_cndmask_b32_e64 v16, v87, v195, s[0:1]
	v_readlane_b32 s0, v249, 49
	v_readlane_b32 s1, v249, 50
	s_nop 1
	v_cndmask_b32_e64 v17, v86, v195, s[0:1]
	v_readlane_b32 s0, v249, 51
	v_readlane_b32 s1, v249, 52
	s_nop 1
	v_cndmask_b32_e64 v105, v105, v195, s[0:1]
	v_readlane_b32 s0, v249, 53
	v_readlane_b32 s1, v249, 54
	s_nop 1
	v_cndmask_b32_e64 v104, v104, v195, s[0:1]
	v_readlane_b32 s0, v249, 55
	v_readlane_b32 s1, v249, 56
	s_nop 1
	v_cndmask_b32_e64 v82, v89, v195, s[0:1]
	v_readlane_b32 s0, v249, 57
	v_readlane_b32 s1, v249, 58
	s_nop 1
	v_cndmask_b32_e64 v84, v88, v195, s[0:1]
	v_readlane_b32 s0, v249, 59
	v_readlane_b32 s1, v249, 60
	s_nop 1
	v_cndmask_b32_e64 v98, v107, v195, s[0:1]
	v_readlane_b32 s0, v249, 61
	v_readlane_b32 s1, v249, 62
	s_nop 1
	v_cndmask_b32_e64 v99, v106, v195, s[0:1]
	v_readlane_b32 s0, v249, 63
	v_readlane_b32 s1, v248, 0
	s_nop 1
	v_cndmask_b32_e64 v86, v91, v195, s[0:1]
	v_readlane_b32 s0, v248, 1
	v_readlane_b32 s1, v248, 2
	s_nop 1
	v_cndmask_b32_e64 v89, v90, v195, s[0:1]
	v_readlane_b32 s0, v248, 3
	v_readlane_b32 s1, v248, 4
	s_nop 1
	v_cndmask_b32_e64 v100, v109, v195, s[0:1]
	v_readlane_b32 s0, v248, 5
	v_readlane_b32 s1, v248, 6
	s_nop 1
	v_cndmask_b32_e64 v101, v108, v195, s[0:1]
	v_readlane_b32 s0, v248, 7
	v_readlane_b32 s1, v248, 8
	s_nop 1
	v_cndmask_b32_e64 v83, v93, v195, s[0:1]
	v_readlane_b32 s0, v248, 9
	v_readlane_b32 s1, v248, 10
	s_nop 1
	v_cndmask_b32_e64 v87, v92, v195, s[0:1]
	v_readlane_b32 s0, v248, 11
	v_readlane_b32 s1, v248, 12
	s_nop 1
	v_cndmask_b32_e64 v93, v111, v195, s[0:1]
	v_readlane_b32 s0, v248, 13
	v_readlane_b32 s1, v248, 14
	s_nop 1
	v_cndmask_b32_e64 v102, v110, v195, s[0:1]
	v_readlane_b32 s0, v248, 15
	v_readlane_b32 s1, v248, 16
	s_nop 1
	v_cndmask_b32_e64 v88, v95, v195, s[0:1]
	v_readlane_b32 s0, v248, 17
	v_readlane_b32 s1, v248, 18
	s_nop 1
	v_cndmask_b32_e64 v90, v94, v195, s[0:1]
	v_readlane_b32 s0, v248, 19
	v_readlane_b32 s1, v248, 20
	s_nop 1
	v_cndmask_b32_e64 v94, v113, v195, s[0:1]
	v_readlane_b32 s0, v248, 21
	v_readlane_b32 s1, v248, 22
	s_nop 1
	v_cndmask_b32_e64 v95, v112, v195, s[0:1]
	v_readlane_b32 s0, v248, 23
	v_readlane_b32 s1, v248, 24
	s_nop 1
	v_cndmask_b32_e64 v91, v97, v195, s[0:1]
	v_readlane_b32 s0, v248, 25
	v_readlane_b32 s1, v248, 26
	v_max_f32_e32 v97, v137, v137
	s_nop 0
	v_cndmask_b32_e64 v92, v96, v195, s[0:1]
	v_max_f32_e32 v96, v134, v134
	v_max_f32_e32 v96, v97, v96
	v_max3_f32 v97, v138, v135, v136
	v_max3_f32 v96, v96, v140, v141
	v_max3_f32 v96, v96, v85, v139
	v_max3_f32 v97, v97, v104, v105
	v_max3_f32 v96, v96, v103, v17
	v_max3_f32 v97, v97, v84, v82
	v_max3_f32 v96, v96, v16, v99
	v_max3_f32 v97, v97, v101, v100
	v_max3_f32 v96, v96, v98, v89
	v_max3_f32 v97, v97, v87, v83
	v_max3_f32 v96, v96, v86, v102
	v_max3_f32 v97, v97, v95, v94
	v_max3_f32 v96, v96, v93, v90
	v_max3_f32 v97, v97, v92, v91
	v_max3_f32 v96, v96, v88, v97
	v_mov_b32_e32 v97, v96
	s_nop 1
	v_permlane32_swap_b32_e32 v96, v97
	v_max_f32_e32 v97, v97, v97
	v_max_f32_e32 v96, v96, v96
	v_max_f32_e32 v96, v96, v97
	s_mov_b32 s0, 0x41000000
	v_cmp_lt_f32_e32 vcc, s0, v96
	s_cmp_eq_u64 vcc, 0
	s_cselect_b64 s[0:1], -1, 0
	s_xor_b64 s[86:87], s[84:85], -1
	s_and_b64 s[0:1], s[86:87], s[0:1]
	s_and_b64 vcc, exec, s[0:1]
	s_cbranch_vccnz .LBB0_625
	v_cndmask_b32_e64 v97, 0, v197, s[84:85]
	v_max_f32_e32 v96, v96, v96
	v_max_f32_e32 v97, v96, v97
	v_exp_f32_e64 v96, -v97
	v_add_f32_e32 v3, v3, v97
	v_sub_f32_e32 v137, v137, v97
	v_sub_f32_e32 v134, v134, v97
	v_sub_f32_e32 v138, v138, v97
	v_sub_f32_e32 v135, v135, v97
	v_sub_f32_e32 v139, v139, v97
	v_sub_f32_e32 v103, v103, v97
	v_sub_f32_e32 v104, v104, v97
	v_sub_f32_e32 v105, v105, v97
	v_sub_f32_e32 v99, v99, v97
	v_sub_f32_e32 v98, v98, v97
	v_sub_f32_e32 v101, v101, v97
	v_sub_f32_e32 v100, v100, v97
	v_sub_f32_e32 v102, v102, v97
	v_sub_f32_e32 v93, v93, v97
	v_sub_f32_e32 v95, v95, v97
	v_sub_f32_e32 v94, v94, v97
	v_sub_f32_e32 v140, v140, v97
	v_sub_f32_e32 v136, v136, v97
	v_sub_f32_e32 v141, v141, v97
	v_sub_f32_e32 v85, v85, v97
	v_sub_f32_e32 v17, v17, v97
	v_sub_f32_e32 v16, v16, v97
	v_sub_f32_e32 v84, v84, v97
	v_sub_f32_e32 v82, v82, v97
	v_sub_f32_e32 v89, v89, v97
	v_sub_f32_e32 v86, v86, v97
	v_sub_f32_e32 v87, v87, v97
	v_sub_f32_e32 v83, v83, v97
	v_sub_f32_e32 v90, v90, v97
	v_sub_f32_e32 v88, v88, v97
	v_sub_f32_e32 v92, v92, v97
	v_sub_f32_e32 v91, v91, v97
	v_pk_mul_f32 v[80:81], v[80:81], v[96:97] op_sel_hi:[1,0]
	v_pk_mul_f32 v[78:79], v[78:79], v[96:97] op_sel_hi:[1,0]
	v_pk_mul_f32 v[76:77], v[76:77], v[96:97] op_sel_hi:[1,0]
	v_pk_mul_f32 v[74:75], v[74:75], v[96:97] op_sel_hi:[1,0]
	v_pk_mul_f32 v[72:73], v[72:73], v[96:97] op_sel_hi:[1,0]
	v_pk_mul_f32 v[70:71], v[70:71], v[96:97] op_sel_hi:[1,0]
	v_pk_mul_f32 v[68:69], v[68:69], v[96:97] op_sel_hi:[1,0]
	v_pk_mul_f32 v[66:67], v[66:67], v[96:97] op_sel_hi:[1,0]
	v_pk_mul_f32 v[64:65], v[64:65], v[96:97] op_sel_hi:[1,0]
	v_pk_mul_f32 v[62:63], v[62:63], v[96:97] op_sel_hi:[1,0]
	v_pk_mul_f32 v[60:61], v[60:61], v[96:97] op_sel_hi:[1,0]
	v_pk_mul_f32 v[58:59], v[58:59], v[96:97] op_sel_hi:[1,0]
	v_pk_mul_f32 v[56:57], v[56:57], v[96:97] op_sel_hi:[1,0]
	v_pk_mul_f32 v[54:55], v[54:55], v[96:97] op_sel_hi:[1,0]
	v_pk_mul_f32 v[52:53], v[52:53], v[96:97] op_sel_hi:[1,0]
	v_pk_mul_f32 v[50:51], v[50:51], v[96:97] op_sel_hi:[1,0]
	v_mul_f32_e32 v213, v213, v96
